# hoist row-scalar loads in expert-up, dense-up, expert-down epilogues (counted vmcnt)
# baseline (speedup 1.0000x reference)
; __device__ __forceinline__ float sigm(float x) { return __builtin_amdgcn_rcpf(1.f + __builtin_amdgcn_exp2f(-1.4426950408889634f * x)); }
; __device__ __forceinline__ unsigned pk4_fp8(float a, float b, float c, float d) { int w = 0; w = __builtin_amdgcn_cvt_pk_fp8_f32(a, b, w, false); w = __builtin_amdgcn_cvt_pk_fp8_f32(c, d, w, true); return (unsigned)w; }
; __device__ __forceinline__ u32x4 pack8(f32x4 v0, f32x4 v1) { u32x4 w; w.x = cvt_pk_bf16(v0[0], v0[1]); w.y = cvt_pk_bf16(v0[2], v0[3]); w.z = cvt_pk_bf16(v1[0], v1[1]); w.w = cvt_pk_bf16(v1[2], v1[3]); return w; }
; template <class T> __device__ __forceinline__ void est(T* p, T v) { if constexpr (MK_EPI_NT != 0) __builtin_nontemporal_store(v, p); else *p = v; }
; __device__ __forceinline__ float ss_val(const ss_t* ss, int row) { return (float)ss[row] * (1.f / 16777216.f); }
;     __device__ __forceinline__ void operator()(AccT acc, const Unit& u, int wr, int wc, int fr, int fq) const {
;         const int row0 = u.pm * 256 + wr * 64 + fr, col0 = u.pn * 128 + wc * 32 + 8 * fq;
; #pragma unroll
;         for (int ai = 0; ai < 2; ++ai)
; #pragma unroll
;             for (int m = 0; m < 4; ++m) { const int row = row0 + ai * 128 + m * 16; const float r = (is_rstd ? ((const float*)rs)[row] : rsqrtf(ss_val((const ss_t*)rs, row) * (1.0f / DM) + EPS)) * ascale;
;                 f32x4 o[2];
; #pragma unroll
;                 for (int bj = 0; bj < 2; ++bj) { const f32x4 a = acc[ai][bj][m][0] * r, b = acc[ai][bj][m][1] * r;
; #pragma unroll
;                     for (int j = 0; j < 4; ++j) o[bj][j] = a[j] * sigm(a[j]) * b[j]; }
;                 if constexpr (F8OUT) est((u32x2*)((unsigned char*)O + (size_t)row * ldo + col0), (u32x2)(u32x2){pk4_fp8(o[0][0], o[0][1], o[0][2], o[0][3]), pk4_fp8(o[1][0], o[1][1], o[1][2], o[1][3])});
;                 else est((u32x4*)((bf16_t*)O + (size_t)row * ldo + col0), (u32x4)pack8(o[0], o[1])); }
;     }
.LBB0_1073:
	v_lshl_add_u32 v144, s84, 8, v149
	v_ashrrev_i32_e32 v145, 31, v144
	v_lshl_add_u64 v[146:147], v[144:145], 3, s[6:7]
	global_load_dwordx2 v[248:249], v[146:147], off
	global_load_dwordx2 v[250:251], v[146:147], off offset:128
	global_load_dwordx2 v[252:253], v[146:147], off offset:256
	global_load_dwordx2 v[254:255], v[146:147], off offset:384
	v_readlane_b32 s20, v246, 0
	v_readlane_b32 s21, v246, 1
	v_lshl_or_b32 v142, s9, 7, v151
	v_ashrrev_i32_e32 v143, 31, v142
	s_mov_b64 s[84:85], -1
	s_waitcnt vmcnt(3)
	v_mov_b32_e32 v156, v248
	v_mov_b32_e32 v157, v249
	global_load_dwordx2 v[248:249], v[146:147], off offset:1024
	v_ffbh_u32_e32 v145, v157
	v_min_u32_e32 v145, 32, v145
	v_lshlrev_b64 v[156:157], v145, v[156:157]
	v_min_u32_e32 v148, 1, v156
	v_or_b32_e32 v148, v157, v148
	v_cvt_f32_u32_e32 v148, v148
	v_sub_u32_e32 v145, 32, v145
	v_mov_b32_e32 v156, v126
	v_mov_b32_e32 v157, v122
	v_ldexp_f32 v145, v148, v145
	v_mul_f32_e32 v145, 0x33800000, v145
	v_fmamk_f32 v145, v145, 0x3a000000, v155
	v_cmp_gt_f32_e32 vcc, s96, v145
	v_mul_f32_e32 v148, 0x4b800000, v145
	s_nop 0
	v_cndmask_b32_e32 v145, v145, v148, vcc
	v_rsq_f32_e32 v145, v145
	s_nop 0
	v_mul_f32_e32 v148, 0x45800000, v145
	v_cndmask_b32_e32 v148, v145, v148, vcc
	v_pk_mul_f32 v[156:157], v[156:157], v[148:149] op_sel_hi:[1,0]
	s_nop 0
	v_mul_f32_e32 v122, 0xbfb8aa3b, v157
	v_exp_f32_e32 v122, v122
	s_nop 0
	v_add_f32_e32 v122, 1.0, v122
	v_rcp_f32_e32 v122, v122
	s_nop 0
	v_mul_f32_e32 v122, v157, v122
	v_mul_f32_e32 v126, v156, v122
	v_mov_b32_e32 v122, v127
	v_pk_mul_f32 v[122:123], v[122:123], v[148:149] op_sel_hi:[1,0]
	s_nop 0
	v_mul_f32_e32 v127, 0xbfb8aa3b, v123
	v_exp_f32_e32 v127, v127
	s_nop 0
	v_add_f32_e32 v127, 1.0, v127
	v_rcp_f32_e32 v127, v127
	s_nop 0
	v_mul_f32_e32 v123, v123, v127
	v_mul_f32_e32 v127, v122, v123
	v_mov_b32_e32 v122, v128
	v_mov_b32_e32 v123, v124
	v_pk_mul_f32 v[122:123], v[122:123], v[148:149] op_sel_hi:[1,0]
	s_nop 0
	v_mul_f32_e32 v124, 0xbfb8aa3b, v123
	v_exp_f32_e32 v124, v124
	s_nop 0
	v_add_f32_e32 v124, 1.0, v124
	v_rcp_f32_e32 v124, v124
	s_nop 0
	v_mul_f32_e32 v123, v123, v124
	v_mov_b32_e32 v124, v129
	v_mul_f32_e32 v128, v122, v123
	v_pk_mul_f32 v[122:123], v[124:125], v[148:149] op_sel_hi:[1,0]
	s_nop 0
	v_mul_f32_e32 v124, 0xbfb8aa3b, v123
	v_exp_f32_e32 v124, v124
	s_nop 0
	v_add_f32_e32 v124, 1.0, v124
	v_rcp_f32_e32 v124, v124
	s_nop 0
	v_mul_f32_e32 v123, v123, v124
	v_mul_f32_e32 v124, v122, v123
	v_mov_b32_e32 v122, v118
	v_mov_b32_e32 v123, v114
	v_pk_mul_f32 v[122:123], v[122:123], v[148:149] op_sel_hi:[1,0]
	s_nop 0
	v_mul_f32_e32 v114, 0xbfb8aa3b, v123
	v_exp_f32_e32 v114, v114
	s_nop 0
	v_add_f32_e32 v114, 1.0, v114
	v_rcp_f32_e32 v114, v114
	s_nop 0
	v_mul_f32_e32 v114, v123, v114
	v_mul_f32_e32 v122, v122, v114
	v_mov_b32_e32 v114, v119
	v_pk_mul_f32 v[114:115], v[114:115], v[148:149] op_sel_hi:[1,0]
	v_mov_b32_e32 v119, 0
	v_mul_f32_e32 v118, 0xbfb8aa3b, v115
	v_exp_f32_e32 v118, v118
	s_nop 0
	v_add_f32_e32 v118, 1.0, v118
	v_rcp_f32_e32 v118, v118
	s_nop 0
	v_mul_f32_e32 v115, v115, v118
	v_mul_f32_e32 v123, v114, v115
	v_mov_b32_e32 v114, v120
	v_mov_b32_e32 v115, v116
	v_pk_mul_f32 v[114:115], v[114:115], v[148:149] op_sel_hi:[1,0]
	v_mov_b32_e32 v118, 0
	v_mul_f32_e32 v116, 0xbfb8aa3b, v115
	v_exp_f32_e32 v116, v116
	v_cvt_pk_fp8_f32 v118, v126, v127
	v_cvt_pk_fp8_f32 v119, v122, v123
	v_add_f32_e32 v116, 1.0, v116
	v_rcp_f32_e32 v116, v116
	v_cvt_pk_fp8_f32 v118, v128, v124 op_sel:[0,0,1]
	v_mul_f32_e32 v115, v115, v116
	v_mov_b32_e32 v116, v121
	v_mul_f32_e32 v120, v114, v115
	v_pk_mul_f32 v[114:115], v[116:117], v[148:149] op_sel_hi:[1,0]
	s_nop 0
	v_mul_f32_e32 v116, 0xbfb8aa3b, v115
	v_exp_f32_e32 v116, v116
	s_nop 0
	v_add_f32_e32 v116, 1.0, v116
	v_rcp_f32_e32 v116, v116
	s_nop 0
	v_mul_f32_e32 v115, v115, v116
	v_mul_f32_e32 v121, v114, v115
	v_cvt_pk_fp8_f32 v119, v120, v121 op_sel:[0,0,1]
	v_mov_b64_e32 v[114:115], s[20:21]
	v_mad_i64_i32 v[116:117], s[20:21], v144, s97, v[114:115]
	v_lshl_add_u64 v[116:117], v[116:117], 0, v[142:143]
	global_store_dwordx2 v[116:117], v[118:119], off
	v_or_b32_e32 v116, 16, v144
	v_ashrrev_i32_e32 v117, 31, v116
	v_lshl_add_u64 v[118:119], v[116:117], 3, s[6:7]
	s_nop 0
	v_mov_b32_e32 v120, v110
	v_mov_b32_e32 v121, v106
	s_waitcnt vmcnt(4)
; __device__ __forceinline__ float sigm(float x) { return __builtin_amdgcn_rcpf(1.f + __builtin_amdgcn_exp2f(-1.4426950408889634f * x)); }
; __device__ __forceinline__ unsigned pk4_fp8(float a, float b, float c, float d) { int w = 0; w = __builtin_amdgcn_cvt_pk_fp8_f32(a, b, w, false); w = __builtin_amdgcn_cvt_pk_fp8_f32(c, d, w, true); return (unsigned)w; }
; __device__ __forceinline__ u32x4 pack8(f32x4 v0, f32x4 v1) { u32x4 w; w.x = cvt_pk_bf16(v0[0], v0[1]); w.y = cvt_pk_bf16(v0[2], v0[3]); w.z = cvt_pk_bf16(v1[0], v1[1]); w.w = cvt_pk_bf16(v1[2], v1[3]); return w; }
; template <class T> __device__ __forceinline__ void est(T* p, T v) { if constexpr (MK_EPI_NT != 0) __builtin_nontemporal_store(v, p); else *p = v; }
; __device__ __forceinline__ float ss_val(const ss_t* ss, int row) { return (float)ss[row] * (1.f / 16777216.f); }
;     __device__ __forceinline__ void operator()(AccT acc, const Unit& u, int wr, int wc, int fr, int fq) const {
;         const int row0 = u.pm * 256 + wr * 64 + fr, col0 = u.pn * 128 + wc * 32 + 8 * fq;
; #pragma unroll
;         for (int ai = 0; ai < 2; ++ai)
; #pragma unroll
;             for (int m = 0; m < 4; ++m) { const int row = row0 + ai * 128 + m * 16; const float r = (is_rstd ? ((const float*)rs)[row] : rsqrtf(ss_val((const ss_t*)rs, row) * (1.0f / DM) + EPS)) * ascale;
;                 f32x4 o[2];
; #pragma unroll
;                 for (int bj = 0; bj < 2; ++bj) { const f32x4 a = acc[ai][bj][m][0] * r, b = acc[ai][bj][m][1] * r;
; #pragma unroll
;                     for (int j = 0; j < 4; ++j) o[bj][j] = a[j] * sigm(a[j]) * b[j]; }
;                 if constexpr (F8OUT) est((u32x2*)((unsigned char*)O + (size_t)row * ldo + col0), (u32x2)(u32x2){pk4_fp8(o[0][0], o[0][1], o[0][2], o[0][3]), pk4_fp8(o[1][0], o[1][1], o[1][2], o[1][3])});
;                 else est((u32x4*)((bf16_t*)O + (size_t)row * ldo + col0), (u32x4)pack8(o[0], o[1])); }
;     }
	v_mov_b32_e32 v118, v250
	v_mov_b32_e32 v119, v251
	global_load_dwordx2 v[250:251], v[146:147], off offset:1152
	v_ffbh_u32_e32 v117, v119
	v_min_u32_e32 v117, 32, v117
	v_lshlrev_b64 v[118:119], v117, v[118:119]
	v_min_u32_e32 v118, 1, v118
	v_or_b32_e32 v118, v119, v118
	v_cvt_f32_u32_e32 v118, v118
	v_sub_u32_e32 v117, 32, v117
	v_ldexp_f32 v117, v118, v117
	v_mul_f32_e32 v117, 0x33800000, v117
	v_fmamk_f32 v117, v117, 0x3a000000, v155
	v_cmp_gt_f32_e32 vcc, s96, v117
	v_mul_f32_e32 v118, 0x4b800000, v117
	s_nop 0
	v_cndmask_b32_e32 v117, v117, v118, vcc
	v_rsq_f32_e32 v117, v117
	s_nop 0
	v_mul_f32_e32 v118, 0x45800000, v117
	v_cndmask_b32_e32 v118, v117, v118, vcc
	v_pk_mul_f32 v[120:121], v[120:121], v[118:119] op_sel_hi:[1,0]
	s_nop 0
	v_mul_f32_e32 v106, 0xbfb8aa3b, v121
	v_exp_f32_e32 v106, v106
	s_nop 0
	v_add_f32_e32 v106, 1.0, v106
	v_rcp_f32_e32 v106, v106
	s_nop 0
	v_mul_f32_e32 v106, v121, v106
	v_mul_f32_e32 v110, v120, v106
	v_mov_b32_e32 v106, v111
	v_pk_mul_f32 v[106:107], v[106:107], v[118:119] op_sel_hi:[1,0]
	s_nop 0
	v_mul_f32_e32 v111, 0xbfb8aa3b, v107
	v_exp_f32_e32 v111, v111
	s_nop 0
	v_add_f32_e32 v111, 1.0, v111
	v_rcp_f32_e32 v111, v111
	s_nop 0
	v_mul_f32_e32 v107, v107, v111
	v_mul_f32_e32 v111, v106, v107
	v_mov_b32_e32 v106, v112
	v_mov_b32_e32 v107, v108
	v_pk_mul_f32 v[106:107], v[106:107], v[118:119] op_sel_hi:[1,0]
	s_nop 0
	v_mul_f32_e32 v108, 0xbfb8aa3b, v107
	v_exp_f32_e32 v108, v108
	s_nop 0
	v_add_f32_e32 v108, 1.0, v108
	v_rcp_f32_e32 v108, v108
	s_nop 0
	v_mul_f32_e32 v107, v107, v108
	v_mov_b32_e32 v108, v113
	v_mul_f32_e32 v112, v106, v107
	v_pk_mul_f32 v[106:107], v[108:109], v[118:119] op_sel_hi:[1,0]
	s_nop 0
	v_mul_f32_e32 v108, 0xbfb8aa3b, v107
	v_exp_f32_e32 v108, v108
	s_nop 0
	v_add_f32_e32 v108, 1.0, v108
	v_rcp_f32_e32 v108, v108
	s_nop 0
	v_mul_f32_e32 v107, v107, v108
	v_mul_f32_e32 v108, v106, v107
	v_mov_b32_e32 v106, v102
	v_mov_b32_e32 v107, v98
	v_pk_mul_f32 v[106:107], v[106:107], v[118:119] op_sel_hi:[1,0]
	s_nop 0
	v_mul_f32_e32 v98, 0xbfb8aa3b, v107
	v_exp_f32_e32 v98, v98
	s_nop 0
	v_add_f32_e32 v98, 1.0, v98
	v_rcp_f32_e32 v98, v98
	s_nop 0
	v_mul_f32_e32 v98, v107, v98
	v_mul_f32_e32 v102, v106, v98
	v_mov_b32_e32 v98, v103
	v_pk_mul_f32 v[98:99], v[98:99], v[118:119] op_sel_hi:[1,0]
	s_nop 0
	v_mul_f32_e32 v103, 0xbfb8aa3b, v99
	v_exp_f32_e32 v103, v103
	s_nop 0
	v_add_f32_e32 v103, 1.0, v103
	v_rcp_f32_e32 v103, v103
	s_nop 0
	v_mul_f32_e32 v99, v99, v103
	v_mul_f32_e32 v103, v98, v99
	v_mov_b32_e32 v98, v104
	v_mov_b32_e32 v99, v100
	v_pk_mul_f32 v[98:99], v[98:99], v[118:119] op_sel_hi:[1,0]
	s_nop 0
	v_mul_f32_e32 v100, 0xbfb8aa3b, v99
	v_exp_f32_e32 v100, v100
	s_nop 0
	v_add_f32_e32 v100, 1.0, v100
	v_rcp_f32_e32 v100, v100
	s_nop 0
	v_mul_f32_e32 v99, v99, v100
	v_mov_b32_e32 v100, v105
	v_mul_f32_e32 v104, v98, v99
	v_pk_mul_f32 v[98:99], v[100:101], v[118:119] op_sel_hi:[1,0]
	v_mov_b32_e32 v101, 0
	v_mul_f32_e32 v100, 0xbfb8aa3b, v99
	v_exp_f32_e32 v100, v100
	v_cvt_pk_fp8_f32 v101, v102, v103
	v_mov_b32_e32 v102, v94
	v_mov_b32_e32 v103, v90
	v_add_f32_e32 v100, 1.0, v100
	v_rcp_f32_e32 v100, v100
	s_nop 0
	v_mul_f32_e32 v99, v99, v100
	v_mov_b32_e32 v100, 0
	v_cvt_pk_fp8_f32 v100, v110, v111
	v_mul_f32_e32 v105, v98, v99
	v_cvt_pk_fp8_f32 v101, v104, v105 op_sel:[0,0,1]
	v_mad_i64_i32 v[98:99], s[20:21], v116, s97, v[114:115]
	v_cvt_pk_fp8_f32 v100, v112, v108 op_sel:[0,0,1]
	v_lshl_add_u64 v[98:99], v[98:99], 0, v[142:143]
	global_store_dwordx2 v[98:99], v[100:101], off
	v_or_b32_e32 v98, 32, v144
	v_ashrrev_i32_e32 v99, 31, v98
	v_lshl_add_u64 v[100:101], v[98:99], 3, s[6:7]
	s_nop 0
	s_waitcnt vmcnt(5)
	v_mov_b32_e32 v100, v252
	v_mov_b32_e32 v101, v253
	global_load_dwordx2 v[252:253], v[146:147], off offset:1280
	v_ffbh_u32_e32 v99, v101
	v_min_u32_e32 v99, 32, v99
	v_lshlrev_b64 v[100:101], v99, v[100:101]
	v_min_u32_e32 v100, 1, v100
	v_or_b32_e32 v100, v101, v100
	v_cvt_f32_u32_e32 v100, v100
	v_sub_u32_e32 v99, 32, v99
	v_ldexp_f32 v99, v100, v99
	v_mul_f32_e32 v99, 0x33800000, v99
	v_fmamk_f32 v99, v99, 0x3a000000, v155
	v_cmp_gt_f32_e32 vcc, s96, v99
	v_mul_f32_e32 v100, 0x4b800000, v99
	s_nop 0
	v_cndmask_b32_e32 v99, v99, v100, vcc
	v_rsq_f32_e32 v99, v99
	s_nop 0
	v_mul_f32_e32 v100, 0x45800000, v99
	v_cndmask_b32_e32 v100, v99, v100, vcc
	v_pk_mul_f32 v[102:103], v[102:103], v[100:101] op_sel_hi:[1,0]
	s_nop 0
	v_mul_f32_e32 v90, 0xbfb8aa3b, v103
	v_exp_f32_e32 v90, v90
	s_nop 0
	v_add_f32_e32 v90, 1.0, v90
	v_rcp_f32_e32 v90, v90
	s_nop 0
	v_mul_f32_e32 v90, v103, v90
	v_mul_f32_e32 v94, v102, v90
	v_mov_b32_e32 v90, v95
	v_pk_mul_f32 v[90:91], v[90:91], v[100:101] op_sel_hi:[1,0]
	s_nop 0
	v_mul_f32_e32 v95, 0xbfb8aa3b, v91
	v_exp_f32_e32 v95, v95
	s_nop 0
	v_add_f32_e32 v95, 1.0, v95
	v_rcp_f32_e32 v95, v95
	s_nop 0
	v_mul_f32_e32 v91, v91, v95
	v_mul_f32_e32 v95, v90, v91
	v_mov_b32_e32 v90, v96
	v_mov_b32_e32 v91, v92
	v_pk_mul_f32 v[90:91], v[90:91], v[100:101] op_sel_hi:[1,0]
	s_nop 0
	v_mul_f32_e32 v92, 0xbfb8aa3b, v91
	v_exp_f32_e32 v92, v92
	s_nop 0
	v_add_f32_e32 v92, 1.0, v92
	v_rcp_f32_e32 v92, v92
	s_nop 0
	v_mul_f32_e32 v91, v91, v92
	v_mov_b32_e32 v92, v97
	v_mul_f32_e32 v96, v90, v91
	v_pk_mul_f32 v[90:91], v[92:93], v[100:101] op_sel_hi:[1,0]
	s_nop 0
	v_mul_f32_e32 v92, 0xbfb8aa3b, v91
	v_exp_f32_e32 v92, v92
	s_nop 0
	v_add_f32_e32 v92, 1.0, v92
	v_rcp_f32_e32 v92, v92
	s_nop 0
	v_mul_f32_e32 v91, v91, v92
	v_mul_f32_e32 v92, v90, v91
	v_mov_b32_e32 v90, v86
	v_mov_b32_e32 v91, v82
	v_pk_mul_f32 v[90:91], v[90:91], v[100:101] op_sel_hi:[1,0]
	s_nop 0
	v_mul_f32_e32 v82, 0xbfb8aa3b, v91
	v_exp_f32_e32 v82, v82
	s_nop 0
; __device__ __forceinline__ float sigm(float x) { return __builtin_amdgcn_rcpf(1.f + __builtin_amdgcn_exp2f(-1.4426950408889634f * x)); }
; __device__ __forceinline__ unsigned pk4_fp8(float a, float b, float c, float d) { int w = 0; w = __builtin_amdgcn_cvt_pk_fp8_f32(a, b, w, false); w = __builtin_amdgcn_cvt_pk_fp8_f32(c, d, w, true); return (unsigned)w; }
; __device__ __forceinline__ u32x4 pack8(f32x4 v0, f32x4 v1) { u32x4 w; w.x = cvt_pk_bf16(v0[0], v0[1]); w.y = cvt_pk_bf16(v0[2], v0[3]); w.z = cvt_pk_bf16(v1[0], v1[1]); w.w = cvt_pk_bf16(v1[2], v1[3]); return w; }
; template <class T> __device__ __forceinline__ void est(T* p, T v) { if constexpr (MK_EPI_NT != 0) __builtin_nontemporal_store(v, p); else *p = v; }
; __device__ __forceinline__ float ss_val(const ss_t* ss, int row) { return (float)ss[row] * (1.f / 16777216.f); }
;     __device__ __forceinline__ void operator()(AccT acc, const Unit& u, int wr, int wc, int fr, int fq) const {
;         const int row0 = u.pm * 256 + wr * 64 + fr, col0 = u.pn * 128 + wc * 32 + 8 * fq;
; #pragma unroll
;         for (int ai = 0; ai < 2; ++ai)
; #pragma unroll
;             for (int m = 0; m < 4; ++m) { const int row = row0 + ai * 128 + m * 16; const float r = (is_rstd ? ((const float*)rs)[row] : rsqrtf(ss_val((const ss_t*)rs, row) * (1.0f / DM) + EPS)) * ascale;
;                 f32x4 o[2];
; #pragma unroll
;                 for (int bj = 0; bj < 2; ++bj) { const f32x4 a = acc[ai][bj][m][0] * r, b = acc[ai][bj][m][1] * r;
; #pragma unroll
;                     for (int j = 0; j < 4; ++j) o[bj][j] = a[j] * sigm(a[j]) * b[j]; }
;                 if constexpr (F8OUT) est((u32x2*)((unsigned char*)O + (size_t)row * ldo + col0), (u32x2)(u32x2){pk4_fp8(o[0][0], o[0][1], o[0][2], o[0][3]), pk4_fp8(o[1][0], o[1][1], o[1][2], o[1][3])});
;                 else est((u32x4*)((bf16_t*)O + (size_t)row * ldo + col0), (u32x4)pack8(o[0], o[1])); }
;     }
	v_add_f32_e32 v82, 1.0, v82
	v_rcp_f32_e32 v82, v82
	s_nop 0
	v_mul_f32_e32 v82, v91, v82
	v_mul_f32_e32 v86, v90, v82
	v_mov_b32_e32 v82, v87
	v_pk_mul_f32 v[82:83], v[82:83], v[100:101] op_sel_hi:[1,0]
	s_nop 0
	v_mul_f32_e32 v87, 0xbfb8aa3b, v83
	v_exp_f32_e32 v87, v87
	s_nop 0
	v_add_f32_e32 v87, 1.0, v87
	v_rcp_f32_e32 v87, v87
	s_nop 0
	v_mul_f32_e32 v83, v83, v87
	v_mul_f32_e32 v87, v82, v83
	v_mov_b32_e32 v82, v88
	v_mov_b32_e32 v83, v84
	v_pk_mul_f32 v[82:83], v[82:83], v[100:101] op_sel_hi:[1,0]
	s_nop 0
	v_mul_f32_e32 v84, 0xbfb8aa3b, v83
	v_exp_f32_e32 v84, v84
	s_nop 0
	v_add_f32_e32 v84, 1.0, v84
	v_rcp_f32_e32 v84, v84
	s_nop 0
	v_mul_f32_e32 v83, v83, v84
	v_mov_b32_e32 v84, v89
	v_mul_f32_e32 v88, v82, v83
	v_pk_mul_f32 v[82:83], v[84:85], v[100:101] op_sel_hi:[1,0]
	v_mov_b32_e32 v85, 0
	v_mul_f32_e32 v84, 0xbfb8aa3b, v83
	v_exp_f32_e32 v84, v84
	v_cvt_pk_fp8_f32 v85, v86, v87
	v_mov_b32_e32 v86, v78
	v_mov_b32_e32 v87, v74
	v_add_f32_e32 v84, 1.0, v84
	v_rcp_f32_e32 v84, v84
	s_nop 0
	v_mul_f32_e32 v83, v83, v84
	v_mov_b32_e32 v84, 0
	v_cvt_pk_fp8_f32 v84, v94, v95
	v_mul_f32_e32 v89, v82, v83
	v_cvt_pk_fp8_f32 v85, v88, v89 op_sel:[0,0,1]
	v_mad_i64_i32 v[82:83], s[20:21], v98, s97, v[114:115]
	v_cvt_pk_fp8_f32 v84, v96, v92 op_sel:[0,0,1]
	v_lshl_add_u64 v[82:83], v[82:83], 0, v[142:143]
	global_store_dwordx2 v[82:83], v[84:85], off
	v_or_b32_e32 v82, 48, v144
	v_ashrrev_i32_e32 v83, 31, v82
	v_lshl_add_u64 v[84:85], v[82:83], 3, s[6:7]
	s_nop 0
	s_waitcnt vmcnt(6)
	v_mov_b32_e32 v84, v254
	v_mov_b32_e32 v85, v255
	global_load_dwordx2 v[254:255], v[146:147], off offset:1408
	v_ffbh_u32_e32 v83, v85
	v_min_u32_e32 v83, 32, v83
	v_lshlrev_b64 v[84:85], v83, v[84:85]
	v_min_u32_e32 v84, 1, v84
	v_or_b32_e32 v84, v85, v84
	v_cvt_f32_u32_e32 v84, v84
	v_sub_u32_e32 v83, 32, v83
	v_ldexp_f32 v83, v84, v83
	v_mul_f32_e32 v83, 0x33800000, v83
	v_fmamk_f32 v83, v83, 0x3a000000, v155
	v_cmp_gt_f32_e32 vcc, s96, v83
	v_mul_f32_e32 v84, 0x4b800000, v83
	s_nop 0
	v_cndmask_b32_e32 v83, v83, v84, vcc
	v_rsq_f32_e32 v83, v83
	s_nop 0
	v_mul_f32_e32 v84, 0x45800000, v83
	v_cndmask_b32_e32 v84, v83, v84, vcc
	v_pk_mul_f32 v[86:87], v[86:87], v[84:85] op_sel_hi:[1,0]
	s_nop 0
	v_mul_f32_e32 v74, 0xbfb8aa3b, v87
	v_exp_f32_e32 v74, v74
	s_nop 0
	v_add_f32_e32 v74, 1.0, v74
	v_rcp_f32_e32 v74, v74
	s_nop 0
	v_mul_f32_e32 v74, v87, v74
	v_mul_f32_e32 v78, v86, v74
	v_mov_b32_e32 v74, v79
	v_pk_mul_f32 v[74:75], v[74:75], v[84:85] op_sel_hi:[1,0]
	s_nop 0
	v_mul_f32_e32 v79, 0xbfb8aa3b, v75
	v_exp_f32_e32 v79, v79
	s_nop 0
	v_add_f32_e32 v79, 1.0, v79
	v_rcp_f32_e32 v79, v79
	s_nop 0
	v_mul_f32_e32 v75, v75, v79
	v_mul_f32_e32 v79, v74, v75
	v_mov_b32_e32 v74, v80
	v_mov_b32_e32 v75, v76
	v_pk_mul_f32 v[74:75], v[74:75], v[84:85] op_sel_hi:[1,0]
	s_nop 0
	v_mul_f32_e32 v76, 0xbfb8aa3b, v75
	v_exp_f32_e32 v76, v76
	s_nop 0
	v_add_f32_e32 v76, 1.0, v76
	v_rcp_f32_e32 v76, v76
	s_nop 0
	v_mul_f32_e32 v75, v75, v76
	v_mov_b32_e32 v76, v81
	v_mul_f32_e32 v80, v74, v75
	v_pk_mul_f32 v[74:75], v[76:77], v[84:85] op_sel_hi:[1,0]
	s_nop 0
	v_mul_f32_e32 v76, 0xbfb8aa3b, v75
	v_exp_f32_e32 v76, v76
	s_nop 0
	v_add_f32_e32 v76, 1.0, v76
	v_rcp_f32_e32 v76, v76
	s_nop 0
	v_mul_f32_e32 v75, v75, v76
	v_mul_f32_e32 v76, v74, v75
	v_mov_b32_e32 v74, v70
	v_mov_b32_e32 v75, v66
	v_pk_mul_f32 v[74:75], v[74:75], v[84:85] op_sel_hi:[1,0]
	s_nop 0
	v_mul_f32_e32 v66, 0xbfb8aa3b, v75
	v_exp_f32_e32 v66, v66
	s_nop 0
	v_add_f32_e32 v66, 1.0, v66
	v_rcp_f32_e32 v66, v66
	s_nop 0
	v_mul_f32_e32 v66, v75, v66
	v_mul_f32_e32 v70, v74, v66
	v_mov_b32_e32 v66, v71
	v_pk_mul_f32 v[66:67], v[66:67], v[84:85] op_sel_hi:[1,0]
	s_nop 0
	v_mul_f32_e32 v71, 0xbfb8aa3b, v67
	v_exp_f32_e32 v71, v71
	s_nop 0
	v_add_f32_e32 v71, 1.0, v71
	v_rcp_f32_e32 v71, v71
	s_nop 0
	v_mul_f32_e32 v67, v67, v71
	v_mul_f32_e32 v71, v66, v67
	v_mov_b32_e32 v66, v72
	v_mov_b32_e32 v67, v68
	v_pk_mul_f32 v[66:67], v[66:67], v[84:85] op_sel_hi:[1,0]
	s_nop 0
	v_mul_f32_e32 v68, 0xbfb8aa3b, v67
	v_exp_f32_e32 v68, v68
	s_nop 0
	v_add_f32_e32 v68, 1.0, v68
	v_rcp_f32_e32 v68, v68
	s_nop 0
	v_mul_f32_e32 v67, v67, v68
	v_mov_b32_e32 v68, v73
	v_mul_f32_e32 v72, v66, v67
	v_pk_mul_f32 v[66:67], v[68:69], v[84:85] op_sel_hi:[1,0]
	v_mov_b32_e32 v69, 0
	v_mul_f32_e32 v68, 0xbfb8aa3b, v67
	v_exp_f32_e32 v68, v68
	v_cvt_pk_fp8_f32 v69, v70, v71
	v_add_u32_e32 v70, 0x80, v144
	v_add_f32_e32 v68, 1.0, v68
	v_rcp_f32_e32 v68, v68
	s_nop 0
	v_mul_f32_e32 v67, v67, v68
	v_mov_b32_e32 v68, 0
	v_cvt_pk_fp8_f32 v68, v78, v79
	v_mul_f32_e32 v73, v66, v67
	v_cvt_pk_fp8_f32 v69, v72, v73 op_sel:[0,0,1]
	v_mad_i64_i32 v[66:67], s[20:21], v82, s97, v[114:115]
	v_cvt_pk_fp8_f32 v68, v80, v76 op_sel:[0,0,1]
	v_lshl_add_u64 v[66:67], v[66:67], 0, v[142:143]
	global_store_dwordx2 v[66:67], v[68:69], off
	s_nop 0
	v_mov_b32_e32 v69, v58
	s_waitcnt vmcnt(7)
; __device__ __forceinline__ float sigm(float x) { return __builtin_amdgcn_rcpf(1.f + __builtin_amdgcn_exp2f(-1.4426950408889634f * x)); }
; __device__ __forceinline__ unsigned pk4_fp8(float a, float b, float c, float d) { int w = 0; w = __builtin_amdgcn_cvt_pk_fp8_f32(a, b, w, false); w = __builtin_amdgcn_cvt_pk_fp8_f32(c, d, w, true); return (unsigned)w; }
; __device__ __forceinline__ u32x4 pack8(f32x4 v0, f32x4 v1) { u32x4 w; w.x = cvt_pk_bf16(v0[0], v0[1]); w.y = cvt_pk_bf16(v0[2], v0[3]); w.z = cvt_pk_bf16(v1[0], v1[1]); w.w = cvt_pk_bf16(v1[2], v1[3]); return w; }
; template <class T> __device__ __forceinline__ void est(T* p, T v) { if constexpr (MK_EPI_NT != 0) __builtin_nontemporal_store(v, p); else *p = v; }
; __device__ __forceinline__ float ss_val(const ss_t* ss, int row) { return (float)ss[row] * (1.f / 16777216.f); }
;     __device__ __forceinline__ void operator()(AccT acc, const Unit& u, int wr, int wc, int fr, int fq) const {
;         const int row0 = u.pm * 256 + wr * 64 + fr, col0 = u.pn * 128 + wc * 32 + 8 * fq;
; #pragma unroll
;         for (int ai = 0; ai < 2; ++ai)
; #pragma unroll
;             for (int m = 0; m < 4; ++m) { const int row = row0 + ai * 128 + m * 16; const float r = (is_rstd ? ((const float*)rs)[row] : rsqrtf(ss_val((const ss_t*)rs, row) * (1.0f / DM) + EPS)) * ascale;
;                 f32x4 o[2];
; #pragma unroll
;                 for (int bj = 0; bj < 2; ++bj) { const f32x4 a = acc[ai][bj][m][0] * r, b = acc[ai][bj][m][1] * r;
; #pragma unroll
;                     for (int j = 0; j < 4; ++j) o[bj][j] = a[j] * sigm(a[j]) * b[j]; }
;                 if constexpr (F8OUT) est((u32x2*)((unsigned char*)O + (size_t)row * ldo + col0), (u32x2)(u32x2){pk4_fp8(o[0][0], o[0][1], o[0][2], o[0][3]), pk4_fp8(o[1][0], o[1][1], o[1][2], o[1][3])});
;                 else est((u32x4*)((bf16_t*)O + (size_t)row * ldo + col0), (u32x4)pack8(o[0], o[1])); }
;     }
	v_mov_b32_e32 v66, v248
	v_mov_b32_e32 v67, v249
	v_ffbh_u32_e32 v68, v67
	v_min_u32_e32 v68, 32, v68
	v_lshlrev_b64 v[66:67], v68, v[66:67]
	v_min_u32_e32 v66, 1, v66
	v_or_b32_e32 v66, v67, v66
	v_cvt_f32_u32_e32 v66, v66
	v_sub_u32_e32 v67, 32, v68
	v_mov_b32_e32 v68, v62
	v_ldexp_f32 v66, v66, v67
	v_mul_f32_e32 v66, 0x33800000, v66
	v_fmamk_f32 v66, v66, 0x3a000000, v155
	v_cmp_gt_f32_e32 vcc, s96, v66
	v_mul_f32_e32 v67, 0x4b800000, v66
	s_nop 0
	v_cndmask_b32_e32 v66, v66, v67, vcc
	v_rsq_f32_e32 v66, v66
	s_nop 0
	v_mul_f32_e32 v67, 0x45800000, v66
	v_cndmask_b32_e32 v66, v66, v67, vcc
	v_pk_mul_f32 v[68:69], v[68:69], v[66:67] op_sel_hi:[1,0]
	s_nop 0
	v_mul_f32_e32 v58, 0xbfb8aa3b, v69
	v_exp_f32_e32 v58, v58
	s_nop 0
	v_add_f32_e32 v58, 1.0, v58
	v_rcp_f32_e32 v58, v58
	s_nop 0
	v_mul_f32_e32 v58, v69, v58
	v_mul_f32_e32 v62, v68, v58
	v_mov_b32_e32 v58, v63
	v_pk_mul_f32 v[58:59], v[58:59], v[66:67] op_sel_hi:[1,0]
	s_nop 0
	v_mul_f32_e32 v63, 0xbfb8aa3b, v59
	v_exp_f32_e32 v63, v63
	s_nop 0
	v_add_f32_e32 v63, 1.0, v63
	v_rcp_f32_e32 v63, v63
	s_nop 0
	v_mul_f32_e32 v59, v59, v63
	v_mul_f32_e32 v63, v58, v59
	v_mov_b32_e32 v58, v64
	v_mov_b32_e32 v59, v60
	v_pk_mul_f32 v[58:59], v[58:59], v[66:67] op_sel_hi:[1,0]
	s_nop 0
	v_mul_f32_e32 v60, 0xbfb8aa3b, v59
	v_exp_f32_e32 v60, v60
	s_nop 0
	v_add_f32_e32 v60, 1.0, v60
	v_rcp_f32_e32 v60, v60
	s_nop 0
	v_mul_f32_e32 v59, v59, v60
	v_mov_b32_e32 v60, v65
	v_mul_f32_e32 v64, v58, v59
	v_pk_mul_f32 v[58:59], v[60:61], v[66:67] op_sel_hi:[1,0]
	s_nop 0
	v_mul_f32_e32 v60, 0xbfb8aa3b, v59
	v_exp_f32_e32 v60, v60
	s_nop 0
	v_add_f32_e32 v60, 1.0, v60
	v_rcp_f32_e32 v60, v60
	s_nop 0
	v_mul_f32_e32 v59, v59, v60
	v_mul_f32_e32 v60, v58, v59
	v_mov_b32_e32 v58, v54
	v_mov_b32_e32 v59, v50
	v_pk_mul_f32 v[58:59], v[58:59], v[66:67] op_sel_hi:[1,0]
	s_nop 0
	v_mul_f32_e32 v50, 0xbfb8aa3b, v59
	v_exp_f32_e32 v50, v50
	s_nop 0
	v_add_f32_e32 v50, 1.0, v50
	v_rcp_f32_e32 v50, v50
	s_nop 0
	v_mul_f32_e32 v50, v59, v50
	v_mul_f32_e32 v54, v58, v50
	v_mov_b32_e32 v50, v55
	v_pk_mul_f32 v[50:51], v[50:51], v[66:67] op_sel_hi:[1,0]
	s_nop 0
	v_mul_f32_e32 v55, 0xbfb8aa3b, v51
	v_exp_f32_e32 v55, v55
	s_nop 0
	v_add_f32_e32 v55, 1.0, v55
	v_rcp_f32_e32 v55, v55
	s_nop 0
	v_mul_f32_e32 v51, v51, v55
	v_mul_f32_e32 v55, v50, v51
	v_mov_b32_e32 v50, v56
	v_mov_b32_e32 v51, v52
	v_pk_mul_f32 v[50:51], v[50:51], v[66:67] op_sel_hi:[1,0]
	s_nop 0
	v_mul_f32_e32 v52, 0xbfb8aa3b, v51
	v_exp_f32_e32 v52, v52
	s_nop 0
	v_add_f32_e32 v52, 1.0, v52
	v_rcp_f32_e32 v52, v52
	s_nop 0
	v_mul_f32_e32 v51, v51, v52
	v_mov_b32_e32 v52, v57
	v_mul_f32_e32 v56, v50, v51
	v_pk_mul_f32 v[50:51], v[52:53], v[66:67] op_sel_hi:[1,0]
	v_mov_b32_e32 v53, 0
	v_mul_f32_e32 v52, 0xbfb8aa3b, v51
	v_exp_f32_e32 v52, v52
	v_cvt_pk_fp8_f32 v53, v54, v55
	v_add_u32_e32 v54, 0x90, v144
	v_add_f32_e32 v52, 1.0, v52
	v_rcp_f32_e32 v52, v52
	s_nop 0
	v_mul_f32_e32 v51, v51, v52
	v_mov_b32_e32 v52, 0
	v_cvt_pk_fp8_f32 v52, v62, v63
	v_mul_f32_e32 v57, v50, v51
	v_cvt_pk_fp8_f32 v53, v56, v57 op_sel:[0,0,1]
	v_mad_i64_i32 v[50:51], s[20:21], v70, s97, v[114:115]
	v_cvt_pk_fp8_f32 v52, v64, v60 op_sel:[0,0,1]
	v_lshl_add_u64 v[50:51], v[50:51], 0, v[142:143]
	global_store_dwordx2 v[50:51], v[52:53], off
	s_nop 0
	v_mov_b32_e32 v53, v42
	s_waitcnt vmcnt(6)
	v_mov_b32_e32 v50, v250
	v_mov_b32_e32 v51, v251
	v_ffbh_u32_e32 v52, v51
	v_min_u32_e32 v52, 32, v52
	v_lshlrev_b64 v[50:51], v52, v[50:51]
	v_min_u32_e32 v50, 1, v50
	v_or_b32_e32 v50, v51, v50
	v_cvt_f32_u32_e32 v50, v50
	v_sub_u32_e32 v51, 32, v52
	v_mov_b32_e32 v52, v46
	v_ldexp_f32 v50, v50, v51
	v_mul_f32_e32 v50, 0x33800000, v50
	v_fmamk_f32 v50, v50, 0x3a000000, v155
	v_cmp_gt_f32_e32 vcc, s96, v50
	v_mul_f32_e32 v51, 0x4b800000, v50
	s_nop 0
	v_cndmask_b32_e32 v50, v50, v51, vcc
	v_rsq_f32_e32 v50, v50
	s_nop 0
	v_mul_f32_e32 v51, 0x45800000, v50
	v_cndmask_b32_e32 v50, v50, v51, vcc
	v_pk_mul_f32 v[52:53], v[52:53], v[50:51] op_sel_hi:[1,0]
	s_nop 0
	v_mul_f32_e32 v42, 0xbfb8aa3b, v53
	v_exp_f32_e32 v42, v42
	s_nop 0
	v_add_f32_e32 v42, 1.0, v42
	v_rcp_f32_e32 v42, v42
	s_nop 0
	v_mul_f32_e32 v42, v53, v42
	v_mul_f32_e32 v46, v52, v42
	v_mov_b32_e32 v42, v47
	v_pk_mul_f32 v[42:43], v[42:43], v[50:51] op_sel_hi:[1,0]
	s_nop 0
	v_mul_f32_e32 v47, 0xbfb8aa3b, v43
	v_exp_f32_e32 v47, v47
	s_nop 0
	v_add_f32_e32 v47, 1.0, v47
	v_rcp_f32_e32 v47, v47
	s_nop 0
	v_mul_f32_e32 v43, v43, v47
	v_mul_f32_e32 v47, v42, v43
	v_mov_b32_e32 v42, v48
	v_mov_b32_e32 v43, v44
	v_pk_mul_f32 v[42:43], v[42:43], v[50:51] op_sel_hi:[1,0]
	s_nop 0
	v_mul_f32_e32 v44, 0xbfb8aa3b, v43
	v_exp_f32_e32 v44, v44
	s_nop 0
	v_add_f32_e32 v44, 1.0, v44
	v_rcp_f32_e32 v44, v44
	s_nop 0
	v_mul_f32_e32 v43, v43, v44
	v_mov_b32_e32 v44, v49
	v_mul_f32_e32 v48, v42, v43
	v_pk_mul_f32 v[42:43], v[44:45], v[50:51] op_sel_hi:[1,0]
	s_nop 0
	v_mul_f32_e32 v44, 0xbfb8aa3b, v43
	v_exp_f32_e32 v44, v44
	s_nop 0
	v_add_f32_e32 v44, 1.0, v44
	v_rcp_f32_e32 v44, v44
	s_nop 0
	v_mul_f32_e32 v43, v43, v44
	v_mul_f32_e32 v44, v42, v43
	v_mov_b32_e32 v42, v38
	v_mov_b32_e32 v43, v34
	v_pk_mul_f32 v[42:43], v[42:43], v[50:51] op_sel_hi:[1,0]
	s_nop 0
	v_mul_f32_e32 v34, 0xbfb8aa3b, v43
	v_exp_f32_e32 v34, v34
	s_nop 0
	v_add_f32_e32 v34, 1.0, v34
	v_rcp_f32_e32 v34, v34
	s_nop 0
	v_mul_f32_e32 v34, v43, v34
	v_mul_f32_e32 v38, v42, v34
	v_mov_b32_e32 v34, v39
	v_pk_mul_f32 v[34:35], v[34:35], v[50:51] op_sel_hi:[1,0]
	s_nop 0
	v_mul_f32_e32 v39, 0xbfb8aa3b, v35
	v_exp_f32_e32 v39, v39
	s_nop 0
	v_add_f32_e32 v39, 1.0, v39
	v_rcp_f32_e32 v39, v39
	s_nop 0
	v_mul_f32_e32 v35, v35, v39
	v_mul_f32_e32 v39, v34, v35
	v_mov_b32_e32 v34, v40
	v_mov_b32_e32 v35, v36
	v_pk_mul_f32 v[34:35], v[34:35], v[50:51] op_sel_hi:[1,0]
	s_nop 0
	v_mul_f32_e32 v36, 0xbfb8aa3b, v35
	v_exp_f32_e32 v36, v36
	s_nop 0
	v_add_f32_e32 v36, 1.0, v36
	v_rcp_f32_e32 v36, v36
	s_nop 0
	v_mul_f32_e32 v35, v35, v36
	v_mov_b32_e32 v36, v41
	v_mul_f32_e32 v40, v34, v35
	v_pk_mul_f32 v[34:35], v[36:37], v[50:51] op_sel_hi:[1,0]
	v_mov_b32_e32 v37, 0
	v_mul_f32_e32 v36, 0xbfb8aa3b, v35
	v_exp_f32_e32 v36, v36
	v_cvt_pk_fp8_f32 v37, v38, v39
	v_add_u32_e32 v38, 0xa0, v144
	v_add_f32_e32 v36, 1.0, v36
	v_rcp_f32_e32 v36, v36
	s_nop 0
	v_mul_f32_e32 v35, v35, v36
	v_mov_b32_e32 v36, 0
	v_cvt_pk_fp8_f32 v36, v46, v47
	v_mul_f32_e32 v41, v34, v35
	v_cvt_pk_fp8_f32 v37, v40, v41 op_sel:[0,0,1]
	v_mad_i64_i32 v[34:35], s[20:21], v54, s97, v[114:115]
	v_cvt_pk_fp8_f32 v36, v48, v44 op_sel:[0,0,1]
	v_lshl_add_u64 v[34:35], v[34:35], 0, v[142:143]
	global_store_dwordx2 v[34:35], v[36:37], off
	s_nop 0
	v_mov_b32_e32 v37, v26
	s_waitcnt vmcnt(5)
; __device__ __forceinline__ float sigm(float x) { return __builtin_amdgcn_rcpf(1.f + __builtin_amdgcn_exp2f(-1.4426950408889634f * x)); }
; __device__ __forceinline__ unsigned pk4_fp8(float a, float b, float c, float d) { int w = 0; w = __builtin_amdgcn_cvt_pk_fp8_f32(a, b, w, false); w = __builtin_amdgcn_cvt_pk_fp8_f32(c, d, w, true); return (unsigned)w; }
; __device__ __forceinline__ u32x4 pack8(f32x4 v0, f32x4 v1) { u32x4 w; w.x = cvt_pk_bf16(v0[0], v0[1]); w.y = cvt_pk_bf16(v0[2], v0[3]); w.z = cvt_pk_bf16(v1[0], v1[1]); w.w = cvt_pk_bf16(v1[2], v1[3]); return w; }
; template <class T> __device__ __forceinline__ void est(T* p, T v) { if constexpr (MK_EPI_NT != 0) __builtin_nontemporal_store(v, p); else *p = v; }
; __device__ __forceinline__ float ss_val(const ss_t* ss, int row) { return (float)ss[row] * (1.f / 16777216.f); }
;     ...
;         if constexpr (Epi::KEEP) keep = E(acc, cur, wr, wc, fr, fq); else E(acc, cur, wr, wc, fr, fq);
;         if (!has_next) break;
;     __device__ __forceinline__ void operator()(AccT acc, const Unit& u, int wr, int wc, int fr, int fq) const {
;         const int row0 = u.pm * 256 + wr * 64 + fr, col0 = u.pn * 128 + wc * 32 + 8 * fq;
; #pragma unroll
;         for (int ai = 0; ai < 2; ++ai)
; #pragma unroll
;             for (int m = 0; m < 4; ++m) { const int row = row0 + ai * 128 + m * 16; const float r = (is_rstd ? ((const float*)rs)[row] : rsqrtf(ss_val((const ss_t*)rs, row) * (1.0f / DM) + EPS)) * ascale;
;                 f32x4 o[2];
; #pragma unroll
;                 for (int bj = 0; bj < 2; ++bj) { const f32x4 a = acc[ai][bj][m][0] * r, b = acc[ai][bj][m][1] * r;
; #pragma unroll
;                     for (int j = 0; j < 4; ++j) o[bj][j] = a[j] * sigm(a[j]) * b[j]; }
;                 if constexpr (F8OUT) est((u32x2*)((unsigned char*)O + (size_t)row * ldo + col0), (u32x2)(u32x2){pk4_fp8(o[0][0], o[0][1], o[0][2], o[0][3]), pk4_fp8(o[1][0], o[1][1], o[1][2], o[1][3])});
;                 else est((u32x4*)((bf16_t*)O + (size_t)row * ldo + col0), (u32x4)pack8(o[0], o[1])); }
;     }
	v_mov_b32_e32 v34, v252
	v_mov_b32_e32 v35, v253
	v_ffbh_u32_e32 v36, v35
	v_min_u32_e32 v36, 32, v36
	v_lshlrev_b64 v[34:35], v36, v[34:35]
	v_min_u32_e32 v34, 1, v34
	v_or_b32_e32 v34, v35, v34
	v_cvt_f32_u32_e32 v34, v34
	v_sub_u32_e32 v35, 32, v36
	v_mov_b32_e32 v36, v30
	v_ldexp_f32 v34, v34, v35
	v_mul_f32_e32 v34, 0x33800000, v34
	v_fmamk_f32 v34, v34, 0x3a000000, v155
	v_cmp_gt_f32_e32 vcc, s96, v34
	v_mul_f32_e32 v35, 0x4b800000, v34
	s_nop 0
	v_cndmask_b32_e32 v34, v34, v35, vcc
	v_rsq_f32_e32 v34, v34
	s_nop 0
	v_mul_f32_e32 v35, 0x45800000, v34
	v_cndmask_b32_e32 v34, v34, v35, vcc
	v_pk_mul_f32 v[36:37], v[36:37], v[34:35] op_sel_hi:[1,0]
	s_nop 0
	v_mul_f32_e32 v26, 0xbfb8aa3b, v37
	v_exp_f32_e32 v26, v26
	s_nop 0
	v_add_f32_e32 v26, 1.0, v26
	v_rcp_f32_e32 v26, v26
	s_nop 0
	v_mul_f32_e32 v26, v37, v26
	v_mul_f32_e32 v30, v36, v26
	v_mov_b32_e32 v26, v31
	v_pk_mul_f32 v[26:27], v[26:27], v[34:35] op_sel_hi:[1,0]
	s_nop 0
	v_mul_f32_e32 v31, 0xbfb8aa3b, v27
	v_exp_f32_e32 v31, v31
	s_nop 0
	v_add_f32_e32 v31, 1.0, v31
	v_rcp_f32_e32 v31, v31
	s_nop 0
	v_mul_f32_e32 v27, v27, v31
	v_mul_f32_e32 v31, v26, v27
	v_mov_b32_e32 v26, v32
	v_mov_b32_e32 v27, v28
	v_pk_mul_f32 v[26:27], v[26:27], v[34:35] op_sel_hi:[1,0]
	s_nop 0
	v_mul_f32_e32 v28, 0xbfb8aa3b, v27
	v_exp_f32_e32 v28, v28
	s_nop 0
	v_add_f32_e32 v28, 1.0, v28
	v_rcp_f32_e32 v28, v28
	s_nop 0
	v_mul_f32_e32 v27, v27, v28
	v_mov_b32_e32 v28, v33
	v_mul_f32_e32 v32, v26, v27
	v_pk_mul_f32 v[26:27], v[28:29], v[34:35] op_sel_hi:[1,0]
	s_nop 0
	v_mul_f32_e32 v28, 0xbfb8aa3b, v27
	v_exp_f32_e32 v28, v28
	s_nop 0
	v_add_f32_e32 v28, 1.0, v28
	v_rcp_f32_e32 v28, v28
	s_nop 0
	v_mul_f32_e32 v27, v27, v28
	v_mul_f32_e32 v28, v26, v27
	v_mov_b32_e32 v26, v22
	v_mov_b32_e32 v27, v18
	v_pk_mul_f32 v[26:27], v[26:27], v[34:35] op_sel_hi:[1,0]
	s_nop 0
	v_mul_f32_e32 v18, 0xbfb8aa3b, v27
	v_exp_f32_e32 v18, v18
	s_nop 0
	v_add_f32_e32 v18, 1.0, v18
	v_rcp_f32_e32 v18, v18
	s_nop 0
	v_mul_f32_e32 v18, v27, v18
	v_mul_f32_e32 v22, v26, v18
	v_mov_b32_e32 v18, v23
	v_pk_mul_f32 v[18:19], v[18:19], v[34:35] op_sel_hi:[1,0]
	s_nop 0
	v_mul_f32_e32 v23, 0xbfb8aa3b, v19
	v_exp_f32_e32 v23, v23
	s_nop 0
	v_add_f32_e32 v23, 1.0, v23
	v_rcp_f32_e32 v23, v23
	s_nop 0
	v_mul_f32_e32 v19, v19, v23
	v_mul_f32_e32 v23, v18, v19
	v_mov_b32_e32 v18, v24
	v_mov_b32_e32 v19, v20
	v_pk_mul_f32 v[18:19], v[18:19], v[34:35] op_sel_hi:[1,0]
	s_nop 0
	v_mul_f32_e32 v20, 0xbfb8aa3b, v19
	v_exp_f32_e32 v20, v20
	s_nop 0
	v_add_f32_e32 v20, 1.0, v20
	v_rcp_f32_e32 v20, v20
	s_nop 0
	v_mul_f32_e32 v19, v19, v20
	v_mov_b32_e32 v20, v25
	v_mul_f32_e32 v24, v18, v19
	v_pk_mul_f32 v[18:19], v[20:21], v[34:35] op_sel_hi:[1,0]
	v_mov_b32_e32 v21, 0
	v_mul_f32_e32 v20, 0xbfb8aa3b, v19
	v_exp_f32_e32 v20, v20
	v_cvt_pk_fp8_f32 v21, v22, v23
	v_add_u32_e32 v22, 0xb0, v144
	v_add_f32_e32 v20, 1.0, v20
	v_rcp_f32_e32 v20, v20
	s_nop 0
	v_mul_f32_e32 v19, v19, v20
	v_mov_b32_e32 v20, 0
	v_cvt_pk_fp8_f32 v20, v30, v31
	v_mul_f32_e32 v25, v18, v19
	v_cvt_pk_fp8_f32 v21, v24, v25 op_sel:[0,0,1]
	v_mad_i64_i32 v[18:19], s[20:21], v38, s97, v[114:115]
	v_cvt_pk_fp8_f32 v20, v32, v28 op_sel:[0,0,1]
	v_lshl_add_u64 v[18:19], v[18:19], 0, v[142:143]
	global_store_dwordx2 v[18:19], v[20:21], off
	s_nop 0
	v_mov_b32_e32 v21, v10
	s_waitcnt vmcnt(4)
	v_mov_b32_e32 v18, v254
	v_mov_b32_e32 v19, v255
	v_ffbh_u32_e32 v20, v19
	v_min_u32_e32 v20, 32, v20
	v_lshlrev_b64 v[18:19], v20, v[18:19]
	v_min_u32_e32 v18, 1, v18
	v_or_b32_e32 v18, v19, v18
	v_cvt_f32_u32_e32 v18, v18
	v_sub_u32_e32 v19, 32, v20
	v_mov_b32_e32 v20, v14
	v_ldexp_f32 v18, v18, v19
	v_mul_f32_e32 v18, 0x33800000, v18
	v_fmamk_f32 v18, v18, 0x3a000000, v155
	v_cmp_gt_f32_e32 vcc, s96, v18
	v_mul_f32_e32 v19, 0x4b800000, v18
	s_nop 0
	v_cndmask_b32_e32 v18, v18, v19, vcc
	v_rsq_f32_e32 v18, v18
	s_nop 0
	v_mul_f32_e32 v19, 0x45800000, v18
	v_cndmask_b32_e32 v18, v18, v19, vcc
	v_pk_mul_f32 v[20:21], v[20:21], v[18:19] op_sel_hi:[1,0]
	s_andn2_b64 vcc, exec, s[4:5]
	v_mul_f32_e32 v10, 0xbfb8aa3b, v21
	v_exp_f32_e32 v10, v10
	s_nop 0
	v_add_f32_e32 v10, 1.0, v10
	v_rcp_f32_e32 v10, v10
	s_nop 0
	v_mul_f32_e32 v10, v21, v10
	v_mul_f32_e32 v14, v20, v10
	v_mov_b32_e32 v10, v15
	v_pk_mul_f32 v[10:11], v[10:11], v[18:19] op_sel_hi:[1,0]
	s_nop 0
	v_mul_f32_e32 v15, 0xbfb8aa3b, v11
	v_exp_f32_e32 v15, v15
	s_nop 0
	v_add_f32_e32 v15, 1.0, v15
	v_rcp_f32_e32 v15, v15
	s_nop 0
	v_mul_f32_e32 v11, v11, v15
	v_mul_f32_e32 v15, v10, v11
	v_mov_b32_e32 v10, v16
	v_mov_b32_e32 v11, v12
	v_pk_mul_f32 v[10:11], v[10:11], v[18:19] op_sel_hi:[1,0]
	s_nop 0
	v_mul_f32_e32 v12, 0xbfb8aa3b, v11
	v_exp_f32_e32 v12, v12
	s_nop 0
	v_add_f32_e32 v12, 1.0, v12
	v_rcp_f32_e32 v12, v12
	s_nop 0
	v_mul_f32_e32 v11, v11, v12
	v_mov_b32_e32 v12, v17
	v_mul_f32_e32 v16, v10, v11
	v_pk_mul_f32 v[10:11], v[12:13], v[18:19] op_sel_hi:[1,0]
	s_nop 0
	v_mul_f32_e32 v12, 0xbfb8aa3b, v11
	v_exp_f32_e32 v12, v12
	s_nop 0
	v_add_f32_e32 v12, 1.0, v12
	v_rcp_f32_e32 v12, v12
	s_nop 0
	v_mul_f32_e32 v11, v11, v12
	v_mul_f32_e32 v12, v10, v11
	v_mov_b32_e32 v10, v2
	v_mov_b32_e32 v11, v6
	v_pk_mul_f32 v[10:11], v[10:11], v[18:19] op_sel_hi:[1,0]
	v_mov_b32_e32 v6, v3
	v_mul_f32_e32 v2, 0xbfb8aa3b, v11
	v_exp_f32_e32 v2, v2
	s_nop 0
	v_add_f32_e32 v2, 1.0, v2
	v_rcp_f32_e32 v2, v2
	s_nop 0
	v_mul_f32_e32 v2, v11, v2
	v_mul_f32_e32 v10, v10, v2
	v_pk_mul_f32 v[2:3], v[6:7], v[18:19] op_sel_hi:[1,0]
	s_nop 0
	v_mul_f32_e32 v6, 0xbfb8aa3b, v3
	v_exp_f32_e32 v6, v6
	s_nop 0
	v_add_f32_e32 v6, 1.0, v6
	v_rcp_f32_e32 v6, v6
	s_nop 0
	v_mul_f32_e32 v3, v3, v6
	v_mul_f32_e32 v6, v2, v3
	v_mov_b32_e32 v2, v4
	v_mov_b32_e32 v3, v8
	v_pk_mul_f32 v[2:3], v[2:3], v[18:19] op_sel_hi:[1,0]
	v_mov_b32_e32 v8, v5
	v_mul_f32_e32 v4, 0xbfb8aa3b, v3
	v_exp_f32_e32 v4, v4
	v_mov_b32_e32 v5, 0
	v_cvt_pk_fp8_f32 v5, v10, v6
	v_add_f32_e32 v4, 1.0, v4
	v_rcp_f32_e32 v4, v4
	s_nop 0
	v_mul_f32_e32 v3, v3, v4
	v_mul_f32_e32 v7, v2, v3
	v_pk_mul_f32 v[2:3], v[8:9], v[18:19] op_sel_hi:[1,0]
	s_nop 0
	v_mul_f32_e32 v4, 0xbfb8aa3b, v3
	v_exp_f32_e32 v4, v4
	s_nop 0
	v_add_f32_e32 v4, 1.0, v4
	v_rcp_f32_e32 v4, v4
	s_nop 0
	v_mul_f32_e32 v3, v3, v4
	v_mov_b32_e32 v4, 0
	v_cvt_pk_fp8_f32 v4, v14, v15
	v_mul_f32_e32 v8, v2, v3
	v_cvt_pk_fp8_f32 v5, v7, v8 op_sel:[0,0,1]
	v_mad_i64_i32 v[2:3], s[20:21], v22, s97, v[114:115]
	v_cvt_pk_fp8_f32 v4, v16, v12 op_sel:[0,0,1]
	v_lshl_add_u64 v[2:3], v[2:3], 0, v[142:143]
	global_store_dwordx2 v[2:3], v[4:5], off
	s_cbranch_vccnz .LBB0_1065
	s_andn2_b64 vcc, exec, s[14:15]
	s_cbranch_vccnz .LBB0_1064
	s_barrier
	s_branch .LBB0_1064

; __device__ __forceinline__ float sigm(float x) { return __builtin_amdgcn_rcpf(1.f + __builtin_amdgcn_exp2f(-1.4426950408889634f * x)); }
; __device__ __forceinline__ unsigned pk4_fp8(float a, float b, float c, float d) { int w = 0; w = __builtin_amdgcn_cvt_pk_fp8_f32(a, b, w, false); w = __builtin_amdgcn_cvt_pk_fp8_f32(c, d, w, true); return (unsigned)w; }
; __device__ __forceinline__ u32x4 pack8(f32x4 v0, f32x4 v1) { u32x4 w; w.x = cvt_pk_bf16(v0[0], v0[1]); w.y = cvt_pk_bf16(v0[2], v0[3]); w.z = cvt_pk_bf16(v1[0], v1[1]); w.w = cvt_pk_bf16(v1[2], v1[3]); return w; }
; template <class T> __device__ __forceinline__ void est(T* p, T v) { if constexpr (MK_EPI_NT != 0) __builtin_nontemporal_store(v, p); else *p = v; }
; __device__ __forceinline__ float ss_val(const ss_t* ss, int row) { return (float)ss[row] * (1.f / 16777216.f); }
;     __device__ __forceinline__ void operator()(AccT acc, const Unit& u, int wr, int wc, int fr, int fq) const {
;         const int row0 = u.pm * 256 + wr * 64 + fr, col0 = u.pn * 128 + wc * 32 + 8 * fq;
; #pragma unroll
;         for (int ai = 0; ai < 2; ++ai)
; #pragma unroll
;             for (int m = 0; m < 4; ++m) { const int row = row0 + ai * 128 + m * 16; const float r = (is_rstd ? ((const float*)rs)[row] : rsqrtf(ss_val((const ss_t*)rs, row) * (1.0f / DM) + EPS)) * ascale;
;                 f32x4 o[2];
; #pragma unroll
;                 for (int bj = 0; bj < 2; ++bj) { const f32x4 a = acc[ai][bj][m][0] * r, b = acc[ai][bj][m][1] * r;
; #pragma unroll
;                     for (int j = 0; j < 4; ++j) o[bj][j] = a[j] * sigm(a[j]) * b[j]; }
;                 if constexpr (F8OUT) est((u32x2*)((unsigned char*)O + (size_t)row * ldo + col0), (u32x2)(u32x2){pk4_fp8(o[0][0], o[0][1], o[0][2], o[0][3]), pk4_fp8(o[1][0], o[1][1], o[1][2], o[1][3])});
;                 else est((u32x4*)((bf16_t*)O + (size_t)row * ldo + col0), (u32x4)pack8(o[0], o[1])); }
;     }
.LBB0_2262:
	v_lshl_add_u32 v2, s62, 8, v1
	v_ashrrev_i32_e32 v3, 31, v2
	s_nop 15
	s_nop 15
	v_lshl_add_u64 v[8:9], v[2:3], 2, s[14:15]
	global_load_dword v248, v[8:9], off
	global_load_dword v249, v[8:9], off offset:64
	global_load_dword v250, v[8:9], off offset:128
	global_load_dword v251, v[8:9], off offset:192
	global_load_dword v252, v[8:9], off offset:512
	global_load_dword v253, v[8:9], off offset:576
	global_load_dword v254, v[8:9], off offset:640
	global_load_dword v255, v[8:9], off offset:704
	v_mov_b32_e32 v4, v154
	v_mov_b32_e32 v6, v150
	v_mov_b32_e32 v20, v151
	v_mov_b32_e32 v24, v152
	v_mov_b32_e32 v28, 0
	v_mov_b32_e32 v29, 0
	v_mov_b32_e32 v26, v153
	v_or_b32_e32 v32, 16, v2
	v_ashrrev_i32_e32 v33, 31, v32
	s_andn2_b64 vcc, exec, s[4:5]
	s_mov_b64 s[4:5], -1
	s_waitcnt vmcnt(7)
	v_mov_b32_e32 v3, v248
	v_mul_f32_e32 v10, 0x3d000000, v3
	v_mul_f32_e32 v11, v158, v10
	v_mul_f32_e32 v3, 0xbfb8aa3b, v11
	v_exp_f32_e32 v3, v3
	s_nop 0
	v_add_f32_e32 v3, 1.0, v3
	v_rcp_f32_e32 v5, v3
	s_nop 0
	v_pk_mul_f32 v[12:13], v[4:5], v[10:11]
	v_mul_f32_e32 v11, v159, v10
	v_mul_f32_e32 v3, 0xbfb8aa3b, v11
	v_exp_f32_e32 v3, v3
	v_mov_b32_e32 v4, v155
	v_mul_f32_e32 v12, v12, v13
	v_add_f32_e32 v3, 1.0, v3
	v_rcp_f32_e32 v5, v3
	s_nop 0
	v_pk_mul_f32 v[14:15], v[4:5], v[10:11]
	v_mul_f32_e32 v11, v160, v10
	v_mul_f32_e32 v3, 0xbfb8aa3b, v11
	v_exp_f32_e32 v3, v3
	v_mov_b32_e32 v4, v156
	v_add_f32_e32 v3, 1.0, v3
	v_rcp_f32_e32 v5, v3
	s_nop 0
	v_pk_mul_f32 v[16:17], v[4:5], v[10:11]
	v_mul_f32_e32 v11, v161, v10
	v_mul_f32_e32 v3, 0xbfb8aa3b, v11
	v_exp_f32_e32 v3, v3
	v_mov_b32_e32 v4, v157
	v_add_f32_e32 v3, 1.0, v3
	v_rcp_f32_e32 v5, v3
	s_nop 0
	v_pk_mul_f32 v[18:19], v[4:5], v[10:11]
	v_mul_f32_e32 v11, v146, v10
	v_mul_f32_e32 v3, 0xbfb8aa3b, v11
	v_exp_f32_e32 v3, v3
	v_lshl_or_b32 v4, s48, 7, v189
	v_ashrrev_i32_e32 v5, 31, v4
	v_add_f32_e32 v3, 1.0, v3
	v_rcp_f32_e32 v7, v3
	s_nop 0
	v_pk_mul_f32 v[22:23], v[6:7], v[10:11]
	v_mul_f32_e32 v11, v147, v10
	v_mul_f32_e32 v3, 0xbfb8aa3b, v11
	v_exp_f32_e32 v3, v3
	v_mov_b64_e32 v[6:7], s[12:13]
	v_mad_i64_i32 v[30:31], s[64:65], v2, s71, v[6:7]
	v_add_f32_e32 v3, 1.0, v3
	v_rcp_f32_e32 v21, v3
	s_nop 0
	v_pk_mul_f32 v[20:21], v[20:21], v[10:11]
	v_mul_f32_e32 v11, v148, v10
	v_mul_f32_e32 v3, 0xbfb8aa3b, v11
	v_exp_f32_e32 v3, v3
	s_nop 0
	v_add_f32_e32 v3, 1.0, v3
	v_rcp_f32_e32 v25, v3
	v_mul_f32_e32 v3, v14, v15
	v_cvt_pk_fp8_f32 v28, v12, v3
	v_mul_f32_e32 v3, v16, v17
	v_pk_mul_f32 v[12:13], v[24:25], v[10:11]
	v_mul_f32_e32 v11, v149, v10
	v_mul_f32_e32 v14, 0xbfb8aa3b, v11
	v_exp_f32_e32 v14, v14
	v_mul_f32_e32 v15, v18, v19
	v_cvt_pk_fp8_f32 v28, v3, v15 op_sel:[0,0,1]
	v_mul_f32_e32 v3, v22, v23
	v_add_f32_e32 v14, 1.0, v14
	v_rcp_f32_e32 v27, v14
	v_mul_f32_e32 v14, v20, v21
	v_cvt_pk_fp8_f32 v29, v3, v14
	v_mul_f32_e32 v3, v12, v13
	v_pk_mul_f32 v[10:11], v[26:27], v[10:11]
	v_lshl_add_u64 v[12:13], v[32:33], 2, s[14:15]
	v_mul_f32_e32 v10, v10, v11
	v_cvt_pk_fp8_f32 v29, v3, v10 op_sel:[0,0,1]
	v_lshl_add_u64 v[10:11], v[30:31], 0, v[4:5]
	v_mov_b32_e32 v14, v139
	v_mov_b32_e32 v16, v140
	global_store_dwordx2 v[10:11], v[28:29], off
	s_nop 0
	v_mov_b32_e32 v12, v138
	v_mov_b32_e32 v18, v141
	v_mov_b32_e32 v20, v134
	v_mov_b32_e32 v22, v135
	v_mov_b32_e32 v24, v136
	v_mov_b32_e32 v28, 0
	v_mov_b32_e32 v29, 0
	v_mov_b32_e32 v26, v137
	v_or_b32_e32 v30, 32, v2
	v_mad_i64_i32 v[32:33], s[64:65], v32, s71, v[6:7]
	v_ashrrev_i32_e32 v31, 31, v30
	s_waitcnt vmcnt(7)
	v_mov_b32_e32 v3, v249
	v_mul_f32_e32 v10, 0x3d000000, v3
	v_mul_f32_e32 v11, v142, v10
	v_mul_f32_e32 v3, 0xbfb8aa3b, v11
	v_exp_f32_e32 v3, v3
	s_nop 0
	v_add_f32_e32 v3, 1.0, v3
	v_rcp_f32_e32 v13, v3
	s_nop 0
	v_pk_mul_f32 v[12:13], v[12:13], v[10:11]
	v_mul_f32_e32 v11, v143, v10
	v_mul_f32_e32 v3, 0xbfb8aa3b, v11
	v_exp_f32_e32 v3, v3
	v_mul_f32_e32 v12, v12, v13
	v_add_f32_e32 v3, 1.0, v3
	v_rcp_f32_e32 v15, v3
	s_nop 0
	v_pk_mul_f32 v[14:15], v[14:15], v[10:11]
	v_mul_f32_e32 v11, v144, v10
	v_mul_f32_e32 v3, 0xbfb8aa3b, v11
	v_exp_f32_e32 v3, v3
	s_nop 0
	v_add_f32_e32 v3, 1.0, v3
	v_rcp_f32_e32 v17, v3
	s_nop 0
	v_pk_mul_f32 v[16:17], v[16:17], v[10:11]
	v_mul_f32_e32 v11, v145, v10
	v_mul_f32_e32 v3, 0xbfb8aa3b, v11
	v_exp_f32_e32 v3, v3
	s_nop 0
	v_add_f32_e32 v3, 1.0, v3
	v_rcp_f32_e32 v19, v3
	s_nop 0
	v_pk_mul_f32 v[18:19], v[18:19], v[10:11]
	v_mul_f32_e32 v11, v130, v10
	v_mul_f32_e32 v3, 0xbfb8aa3b, v11
	v_exp_f32_e32 v3, v3
	s_nop 0
	v_add_f32_e32 v3, 1.0, v3
	v_rcp_f32_e32 v21, v3
	s_nop 0
	v_pk_mul_f32 v[20:21], v[20:21], v[10:11]
	v_mul_f32_e32 v11, v131, v10
	v_mul_f32_e32 v3, 0xbfb8aa3b, v11
	v_exp_f32_e32 v3, v3
	s_nop 0
	v_add_f32_e32 v3, 1.0, v3
	v_rcp_f32_e32 v23, v3
	s_nop 0
	v_pk_mul_f32 v[22:23], v[22:23], v[10:11]
	v_mul_f32_e32 v11, v132, v10
	v_mul_f32_e32 v3, 0xbfb8aa3b, v11
	v_exp_f32_e32 v3, v3
	s_nop 0
	v_add_f32_e32 v3, 1.0, v3
	v_rcp_f32_e32 v25, v3
	v_mul_f32_e32 v3, v14, v15
	v_cvt_pk_fp8_f32 v28, v12, v3
	v_mul_f32_e32 v3, v16, v17
	v_pk_mul_f32 v[12:13], v[24:25], v[10:11]
	v_mul_f32_e32 v11, v133, v10
	v_mul_f32_e32 v14, 0xbfb8aa3b, v11
	v_exp_f32_e32 v14, v14
	v_mul_f32_e32 v15, v18, v19
	v_cvt_pk_fp8_f32 v28, v3, v15 op_sel:[0,0,1]
	v_mul_f32_e32 v3, v20, v21
	v_add_f32_e32 v14, 1.0, v14
	v_rcp_f32_e32 v27, v14
	v_mul_f32_e32 v14, v22, v23
	v_cvt_pk_fp8_f32 v29, v3, v14
	v_mul_f32_e32 v3, v12, v13
	v_pk_mul_f32 v[10:11], v[26:27], v[10:11]
	v_lshl_add_u64 v[12:13], v[30:31], 2, s[14:15]
	v_mul_f32_e32 v10, v10, v11
	v_cvt_pk_fp8_f32 v29, v3, v10 op_sel:[0,0,1]
	v_lshl_add_u64 v[10:11], v[32:33], 0, v[4:5]
	v_mov_b32_e32 v14, v123
	v_mov_b32_e32 v16, v124
	global_store_dwordx2 v[10:11], v[28:29], off
	s_nop 0
	v_mov_b32_e32 v12, v122
	v_mov_b32_e32 v18, v125
	v_mov_b32_e32 v20, v118
	v_mov_b32_e32 v22, v119
	v_mov_b32_e32 v24, v120
	v_mov_b32_e32 v28, 0
	v_mov_b32_e32 v29, 0
	v_mov_b32_e32 v26, v121
	v_or_b32_e32 v32, 48, v2
	v_mad_i64_i32 v[30:31], s[64:65], v30, s71, v[6:7]
	v_ashrrev_i32_e32 v33, 31, v32
	s_waitcnt vmcnt(7)
; __device__ __forceinline__ float sigm(float x) { return __builtin_amdgcn_rcpf(1.f + __builtin_amdgcn_exp2f(-1.4426950408889634f * x)); }
; __device__ __forceinline__ unsigned pk4_fp8(float a, float b, float c, float d) { int w = 0; w = __builtin_amdgcn_cvt_pk_fp8_f32(a, b, w, false); w = __builtin_amdgcn_cvt_pk_fp8_f32(c, d, w, true); return (unsigned)w; }
; __device__ __forceinline__ u32x4 pack8(f32x4 v0, f32x4 v1) { u32x4 w; w.x = cvt_pk_bf16(v0[0], v0[1]); w.y = cvt_pk_bf16(v0[2], v0[3]); w.z = cvt_pk_bf16(v1[0], v1[1]); w.w = cvt_pk_bf16(v1[2], v1[3]); return w; }
; template <class T> __device__ __forceinline__ void est(T* p, T v) { if constexpr (MK_EPI_NT != 0) __builtin_nontemporal_store(v, p); else *p = v; }
; __device__ __forceinline__ float ss_val(const ss_t* ss, int row) { return (float)ss[row] * (1.f / 16777216.f); }
;     __device__ __forceinline__ void operator()(AccT acc, const Unit& u, int wr, int wc, int fr, int fq) const {
;         const int row0 = u.pm * 256 + wr * 64 + fr, col0 = u.pn * 128 + wc * 32 + 8 * fq;
; #pragma unroll
;         for (int ai = 0; ai < 2; ++ai)
; #pragma unroll
;             for (int m = 0; m < 4; ++m) { const int row = row0 + ai * 128 + m * 16; const float r = (is_rstd ? ((const float*)rs)[row] : rsqrtf(ss_val((const ss_t*)rs, row) * (1.0f / DM) + EPS)) * ascale;
;                 f32x4 o[2];
; #pragma unroll
;                 for (int bj = 0; bj < 2; ++bj) { const f32x4 a = acc[ai][bj][m][0] * r, b = acc[ai][bj][m][1] * r;
; #pragma unroll
;                     for (int j = 0; j < 4; ++j) o[bj][j] = a[j] * sigm(a[j]) * b[j]; }
;                 if constexpr (F8OUT) est((u32x2*)((unsigned char*)O + (size_t)row * ldo + col0), (u32x2)(u32x2){pk4_fp8(o[0][0], o[0][1], o[0][2], o[0][3]), pk4_fp8(o[1][0], o[1][1], o[1][2], o[1][3])});
;                 else est((u32x4*)((bf16_t*)O + (size_t)row * ldo + col0), (u32x4)pack8(o[0], o[1])); }
;     }
	v_mov_b32_e32 v3, v250
	v_mul_f32_e32 v10, 0x3d000000, v3
	v_mul_f32_e32 v11, v126, v10
	v_mul_f32_e32 v3, 0xbfb8aa3b, v11
	v_exp_f32_e32 v3, v3
	s_nop 0
	v_add_f32_e32 v3, 1.0, v3
	v_rcp_f32_e32 v13, v3
	s_nop 0
	v_pk_mul_f32 v[12:13], v[12:13], v[10:11]
	v_mul_f32_e32 v11, v127, v10
	v_mul_f32_e32 v3, 0xbfb8aa3b, v11
	v_exp_f32_e32 v3, v3
	v_mul_f32_e32 v12, v12, v13
	v_add_f32_e32 v3, 1.0, v3
	v_rcp_f32_e32 v15, v3
	s_nop 0
	v_pk_mul_f32 v[14:15], v[14:15], v[10:11]
	v_mul_f32_e32 v11, v128, v10
	v_mul_f32_e32 v3, 0xbfb8aa3b, v11
	v_exp_f32_e32 v3, v3
	s_nop 0
	v_add_f32_e32 v3, 1.0, v3
	v_rcp_f32_e32 v17, v3
	s_nop 0
	v_pk_mul_f32 v[16:17], v[16:17], v[10:11]
	v_mul_f32_e32 v11, v129, v10
	v_mul_f32_e32 v3, 0xbfb8aa3b, v11
	v_exp_f32_e32 v3, v3
	s_nop 0
	v_add_f32_e32 v3, 1.0, v3
	v_rcp_f32_e32 v19, v3
	s_nop 0
	v_pk_mul_f32 v[18:19], v[18:19], v[10:11]
	v_mul_f32_e32 v11, v114, v10
	v_mul_f32_e32 v3, 0xbfb8aa3b, v11
	v_exp_f32_e32 v3, v3
	s_nop 0
	v_add_f32_e32 v3, 1.0, v3
	v_rcp_f32_e32 v21, v3
	s_nop 0
	v_pk_mul_f32 v[20:21], v[20:21], v[10:11]
	v_mul_f32_e32 v11, v115, v10
	v_mul_f32_e32 v3, 0xbfb8aa3b, v11
	v_exp_f32_e32 v3, v3
	s_nop 0
	v_add_f32_e32 v3, 1.0, v3
	v_rcp_f32_e32 v23, v3
	s_nop 0
	v_pk_mul_f32 v[22:23], v[22:23], v[10:11]
	v_mul_f32_e32 v11, v116, v10
	v_mul_f32_e32 v3, 0xbfb8aa3b, v11
	v_exp_f32_e32 v3, v3
	s_nop 0
	v_add_f32_e32 v3, 1.0, v3
	v_rcp_f32_e32 v25, v3
	v_mul_f32_e32 v3, v14, v15
	v_cvt_pk_fp8_f32 v28, v12, v3
	v_mul_f32_e32 v3, v16, v17
	v_pk_mul_f32 v[12:13], v[24:25], v[10:11]
	v_mul_f32_e32 v11, v117, v10
	v_mul_f32_e32 v14, 0xbfb8aa3b, v11
	v_exp_f32_e32 v14, v14
	v_mul_f32_e32 v15, v18, v19
	v_cvt_pk_fp8_f32 v28, v3, v15 op_sel:[0,0,1]
	v_mul_f32_e32 v3, v20, v21
	v_add_f32_e32 v14, 1.0, v14
	v_rcp_f32_e32 v27, v14
	v_mul_f32_e32 v14, v22, v23
	v_cvt_pk_fp8_f32 v29, v3, v14
	v_mul_f32_e32 v3, v12, v13
	v_pk_mul_f32 v[10:11], v[26:27], v[10:11]
	v_lshl_add_u64 v[12:13], v[32:33], 2, s[14:15]
	v_mul_f32_e32 v10, v10, v11
	v_cvt_pk_fp8_f32 v29, v3, v10 op_sel:[0,0,1]
	v_lshl_add_u64 v[10:11], v[30:31], 0, v[4:5]
	v_mov_b32_e32 v14, v107
	v_mov_b32_e32 v16, v108
	global_store_dwordx2 v[10:11], v[28:29], off
	s_nop 0
	v_mov_b32_e32 v12, v106
	v_mov_b32_e32 v18, v109
	v_mov_b32_e32 v20, v102
	v_mov_b32_e32 v22, v103
	v_mov_b32_e32 v24, v104
	v_mov_b32_e32 v28, 0
	v_mov_b32_e32 v29, 0
	v_mov_b32_e32 v26, v105
	v_add_u32_e32 v30, 0x80, v2
	s_waitcnt vmcnt(7)
	v_mov_b32_e32 v3, v251
	v_mul_f32_e32 v10, 0x3d000000, v3
	v_mul_f32_e32 v11, v110, v10
	v_mul_f32_e32 v3, 0xbfb8aa3b, v11
	v_exp_f32_e32 v3, v3
	s_nop 0
	v_add_f32_e32 v3, 1.0, v3
	v_rcp_f32_e32 v13, v3
	s_nop 0
	v_pk_mul_f32 v[12:13], v[12:13], v[10:11]
	v_mul_f32_e32 v11, v111, v10
	v_mul_f32_e32 v3, 0xbfb8aa3b, v11
	v_exp_f32_e32 v3, v3
	v_mul_f32_e32 v12, v12, v13
	v_add_f32_e32 v3, 1.0, v3
	v_rcp_f32_e32 v15, v3
	s_nop 0
	v_pk_mul_f32 v[14:15], v[14:15], v[10:11]
	v_mul_f32_e32 v11, v112, v10
	v_mul_f32_e32 v3, 0xbfb8aa3b, v11
	v_exp_f32_e32 v3, v3
	s_nop 0
	v_add_f32_e32 v3, 1.0, v3
	v_rcp_f32_e32 v17, v3
	s_nop 0
	v_pk_mul_f32 v[16:17], v[16:17], v[10:11]
	v_mul_f32_e32 v11, v113, v10
	v_mul_f32_e32 v3, 0xbfb8aa3b, v11
	v_exp_f32_e32 v3, v3
	s_nop 0
	v_add_f32_e32 v3, 1.0, v3
	v_rcp_f32_e32 v19, v3
	s_nop 0
	v_pk_mul_f32 v[18:19], v[18:19], v[10:11]
	v_mul_f32_e32 v11, v98, v10
	v_mul_f32_e32 v3, 0xbfb8aa3b, v11
	v_exp_f32_e32 v3, v3
	s_nop 0
	v_add_f32_e32 v3, 1.0, v3
	v_rcp_f32_e32 v21, v3
	s_nop 0
	v_pk_mul_f32 v[20:21], v[20:21], v[10:11]
	v_mul_f32_e32 v11, v99, v10
	v_mul_f32_e32 v3, 0xbfb8aa3b, v11
	v_exp_f32_e32 v3, v3
	s_nop 0
	v_add_f32_e32 v3, 1.0, v3
	v_rcp_f32_e32 v23, v3
	s_nop 0
	v_pk_mul_f32 v[22:23], v[22:23], v[10:11]
	v_mul_f32_e32 v11, v100, v10
	v_mul_f32_e32 v3, 0xbfb8aa3b, v11
	v_exp_f32_e32 v3, v3
	s_nop 0
	v_add_f32_e32 v3, 1.0, v3
	v_rcp_f32_e32 v25, v3
	v_mul_f32_e32 v3, v14, v15
	v_cvt_pk_fp8_f32 v28, v12, v3
	v_mul_f32_e32 v3, v16, v17
	v_pk_mul_f32 v[12:13], v[24:25], v[10:11]
	v_mul_f32_e32 v11, v101, v10
	v_mul_f32_e32 v14, 0xbfb8aa3b, v11
	v_exp_f32_e32 v14, v14
	v_mul_f32_e32 v15, v18, v19
	v_cvt_pk_fp8_f32 v28, v3, v15 op_sel:[0,0,1]
	v_mul_f32_e32 v3, v20, v21
	v_add_f32_e32 v14, 1.0, v14
	v_rcp_f32_e32 v27, v14
	v_mul_f32_e32 v14, v22, v23
	v_cvt_pk_fp8_f32 v29, v3, v14
	v_mul_f32_e32 v3, v12, v13
	v_pk_mul_f32 v[10:11], v[26:27], v[10:11]
	v_mov_b32_e32 v12, v90
	v_mul_f32_e32 v10, v10, v11
	v_cvt_pk_fp8_f32 v29, v3, v10 op_sel:[0,0,1]
	v_mad_i64_i32 v[10:11], s[64:65], v32, s71, v[6:7]
	v_lshl_add_u64 v[10:11], v[10:11], 0, v[4:5]
	global_store_dwordx2 v[10:11], v[28:29], off
	s_nop 0
	v_mov_b32_e32 v14, v91
	v_mov_b32_e32 v16, v92
	v_mov_b32_e32 v18, v93
	v_mov_b32_e32 v20, v86
	v_mov_b32_e32 v22, v87
	v_mov_b32_e32 v24, v88
	v_mov_b32_e32 v28, 0
	v_mov_b32_e32 v29, 0
	v_mov_b32_e32 v26, v89
	s_waitcnt vmcnt(7)
; __device__ __forceinline__ float sigm(float x) { return __builtin_amdgcn_rcpf(1.f + __builtin_amdgcn_exp2f(-1.4426950408889634f * x)); }
; __device__ __forceinline__ unsigned pk4_fp8(float a, float b, float c, float d) { int w = 0; w = __builtin_amdgcn_cvt_pk_fp8_f32(a, b, w, false); w = __builtin_amdgcn_cvt_pk_fp8_f32(c, d, w, true); return (unsigned)w; }
; __device__ __forceinline__ u32x4 pack8(f32x4 v0, f32x4 v1) { u32x4 w; w.x = cvt_pk_bf16(v0[0], v0[1]); w.y = cvt_pk_bf16(v0[2], v0[3]); w.z = cvt_pk_bf16(v1[0], v1[1]); w.w = cvt_pk_bf16(v1[2], v1[3]); return w; }
; template <class T> __device__ __forceinline__ void est(T* p, T v) { if constexpr (MK_EPI_NT != 0) __builtin_nontemporal_store(v, p); else *p = v; }
; __device__ __forceinline__ float ss_val(const ss_t* ss, int row) { return (float)ss[row] * (1.f / 16777216.f); }
;     __device__ __forceinline__ void operator()(AccT acc, const Unit& u, int wr, int wc, int fr, int fq) const {
;         const int row0 = u.pm * 256 + wr * 64 + fr, col0 = u.pn * 128 + wc * 32 + 8 * fq;
; #pragma unroll
;         for (int ai = 0; ai < 2; ++ai)
; #pragma unroll
;             for (int m = 0; m < 4; ++m) { const int row = row0 + ai * 128 + m * 16; const float r = (is_rstd ? ((const float*)rs)[row] : rsqrtf(ss_val((const ss_t*)rs, row) * (1.0f / DM) + EPS)) * ascale;
;                 f32x4 o[2];
; #pragma unroll
;                 for (int bj = 0; bj < 2; ++bj) { const f32x4 a = acc[ai][bj][m][0] * r, b = acc[ai][bj][m][1] * r;
; #pragma unroll
;                     for (int j = 0; j < 4; ++j) o[bj][j] = a[j] * sigm(a[j]) * b[j]; }
;                 if constexpr (F8OUT) est((u32x2*)((unsigned char*)O + (size_t)row * ldo + col0), (u32x2)(u32x2){pk4_fp8(o[0][0], o[0][1], o[0][2], o[0][3]), pk4_fp8(o[1][0], o[1][1], o[1][2], o[1][3])});
;                 else est((u32x4*)((bf16_t*)O + (size_t)row * ldo + col0), (u32x4)pack8(o[0], o[1])); }
;     }
	v_mov_b32_e32 v3, v252
	v_mul_f32_e32 v10, 0x3d000000, v3
	v_mul_f32_e32 v11, v94, v10
	v_mul_f32_e32 v3, 0xbfb8aa3b, v11
	v_exp_f32_e32 v3, v3
	s_nop 0
	v_add_f32_e32 v3, 1.0, v3
	v_rcp_f32_e32 v13, v3
	s_nop 0
	v_pk_mul_f32 v[12:13], v[12:13], v[10:11]
	v_mul_f32_e32 v11, v95, v10
	v_mul_f32_e32 v3, 0xbfb8aa3b, v11
	v_exp_f32_e32 v3, v3
	v_mul_f32_e32 v12, v12, v13
	v_add_f32_e32 v3, 1.0, v3
	v_rcp_f32_e32 v15, v3
	s_nop 0
	v_pk_mul_f32 v[14:15], v[14:15], v[10:11]
	v_mul_f32_e32 v11, v96, v10
	v_mul_f32_e32 v3, 0xbfb8aa3b, v11
	v_exp_f32_e32 v3, v3
	s_nop 0
	v_add_f32_e32 v3, 1.0, v3
	v_rcp_f32_e32 v17, v3
	s_nop 0
	v_pk_mul_f32 v[16:17], v[16:17], v[10:11]
	v_mul_f32_e32 v11, v97, v10
	v_mul_f32_e32 v3, 0xbfb8aa3b, v11
	v_exp_f32_e32 v3, v3
	s_nop 0
	v_add_f32_e32 v3, 1.0, v3
	v_rcp_f32_e32 v19, v3
	s_nop 0
	v_pk_mul_f32 v[18:19], v[18:19], v[10:11]
	v_mul_f32_e32 v11, v82, v10
	v_mul_f32_e32 v3, 0xbfb8aa3b, v11
	v_exp_f32_e32 v3, v3
	s_nop 0
	v_add_f32_e32 v3, 1.0, v3
	v_rcp_f32_e32 v21, v3
	s_nop 0
	v_pk_mul_f32 v[20:21], v[20:21], v[10:11]
	v_mul_f32_e32 v11, v83, v10
	v_mul_f32_e32 v3, 0xbfb8aa3b, v11
	v_exp_f32_e32 v3, v3
	s_nop 0
	v_add_f32_e32 v3, 1.0, v3
	v_rcp_f32_e32 v23, v3
	s_nop 0
	v_pk_mul_f32 v[22:23], v[22:23], v[10:11]
	v_mul_f32_e32 v11, v84, v10
	v_mul_f32_e32 v3, 0xbfb8aa3b, v11
	v_exp_f32_e32 v3, v3
	s_nop 0
	v_add_f32_e32 v3, 1.0, v3
	v_rcp_f32_e32 v25, v3
	v_mul_f32_e32 v3, v14, v15
	v_cvt_pk_fp8_f32 v28, v12, v3
	v_mul_f32_e32 v3, v16, v17
	v_pk_mul_f32 v[12:13], v[24:25], v[10:11]
	v_mul_f32_e32 v11, v85, v10
	v_mul_f32_e32 v14, 0xbfb8aa3b, v11
	v_exp_f32_e32 v14, v14
	v_mul_f32_e32 v15, v18, v19
	v_cvt_pk_fp8_f32 v28, v3, v15 op_sel:[0,0,1]
	v_mul_f32_e32 v3, v20, v21
	v_add_f32_e32 v14, 1.0, v14
	v_rcp_f32_e32 v27, v14
	v_mul_f32_e32 v14, v22, v23
	v_cvt_pk_fp8_f32 v29, v3, v14
	v_mul_f32_e32 v3, v12, v13
	v_pk_mul_f32 v[10:11], v[26:27], v[10:11]
	v_mov_b32_e32 v12, v74
	v_mul_f32_e32 v10, v10, v11
	v_cvt_pk_fp8_f32 v29, v3, v10 op_sel:[0,0,1]
	v_mad_i64_i32 v[10:11], s[64:65], v30, s71, v[6:7]
	v_lshl_add_u64 v[10:11], v[10:11], 0, v[4:5]
	global_store_dwordx2 v[10:11], v[28:29], off
	s_nop 0
	v_mov_b32_e32 v14, v75
	v_mov_b32_e32 v16, v76
	v_mov_b32_e32 v18, v77
	v_mov_b32_e32 v20, v70
	v_mov_b32_e32 v22, v71
	v_mov_b32_e32 v24, v72
	v_mov_b32_e32 v28, 0
	v_mov_b32_e32 v29, 0
	v_mov_b32_e32 v26, v73
	v_add_u32_e32 v30, 0x90, v2
	s_waitcnt vmcnt(7)
	v_mov_b32_e32 v3, v253
	v_mul_f32_e32 v10, 0x3d000000, v3
	v_mul_f32_e32 v11, v78, v10
	v_mul_f32_e32 v3, 0xbfb8aa3b, v11
	v_exp_f32_e32 v3, v3
	s_nop 0
	v_add_f32_e32 v3, 1.0, v3
	v_rcp_f32_e32 v13, v3
	s_nop 0
	v_pk_mul_f32 v[12:13], v[12:13], v[10:11]
	v_mul_f32_e32 v11, v79, v10
	v_mul_f32_e32 v3, 0xbfb8aa3b, v11
	v_exp_f32_e32 v3, v3
	v_mul_f32_e32 v12, v12, v13
	v_add_f32_e32 v3, 1.0, v3
	v_rcp_f32_e32 v15, v3
	s_nop 0
	v_pk_mul_f32 v[14:15], v[14:15], v[10:11]
	v_mul_f32_e32 v11, v80, v10
	v_mul_f32_e32 v3, 0xbfb8aa3b, v11
	v_exp_f32_e32 v3, v3
	s_nop 0
	v_add_f32_e32 v3, 1.0, v3
	v_rcp_f32_e32 v17, v3
	s_nop 0
	v_pk_mul_f32 v[16:17], v[16:17], v[10:11]
	v_mul_f32_e32 v11, v81, v10
	v_mul_f32_e32 v3, 0xbfb8aa3b, v11
	v_exp_f32_e32 v3, v3
	s_nop 0
	v_add_f32_e32 v3, 1.0, v3
	v_rcp_f32_e32 v19, v3
	s_nop 0
	v_pk_mul_f32 v[18:19], v[18:19], v[10:11]
	v_mul_f32_e32 v11, v66, v10
	v_mul_f32_e32 v3, 0xbfb8aa3b, v11
	v_exp_f32_e32 v3, v3
	s_nop 0
	v_add_f32_e32 v3, 1.0, v3
	v_rcp_f32_e32 v21, v3
	s_nop 0
	v_pk_mul_f32 v[20:21], v[20:21], v[10:11]
	v_mul_f32_e32 v11, v67, v10
	v_mul_f32_e32 v3, 0xbfb8aa3b, v11
	v_exp_f32_e32 v3, v3
	s_nop 0
	v_add_f32_e32 v3, 1.0, v3
	v_rcp_f32_e32 v23, v3
	s_nop 0
	v_pk_mul_f32 v[22:23], v[22:23], v[10:11]
	v_mul_f32_e32 v11, v68, v10
	v_mul_f32_e32 v3, 0xbfb8aa3b, v11
	v_exp_f32_e32 v3, v3
	s_nop 0
	v_add_f32_e32 v3, 1.0, v3
	v_rcp_f32_e32 v25, v3
	v_mul_f32_e32 v3, v14, v15
	v_cvt_pk_fp8_f32 v28, v12, v3
	v_mul_f32_e32 v3, v16, v17
	v_pk_mul_f32 v[12:13], v[24:25], v[10:11]
	v_mul_f32_e32 v11, v69, v10
	v_mul_f32_e32 v14, 0xbfb8aa3b, v11
	v_exp_f32_e32 v14, v14
	v_mul_f32_e32 v15, v18, v19
	v_cvt_pk_fp8_f32 v28, v3, v15 op_sel:[0,0,1]
	v_mul_f32_e32 v3, v20, v21
	v_add_f32_e32 v14, 1.0, v14
	v_rcp_f32_e32 v27, v14
	v_mul_f32_e32 v14, v22, v23
	v_cvt_pk_fp8_f32 v29, v3, v14
	v_mul_f32_e32 v3, v12, v13
	v_pk_mul_f32 v[10:11], v[26:27], v[10:11]
	v_mov_b32_e32 v12, v58
	v_mul_f32_e32 v10, v10, v11
	v_cvt_pk_fp8_f32 v29, v3, v10 op_sel:[0,0,1]
	v_mad_i64_i32 v[10:11], s[64:65], v30, s71, v[6:7]
	v_lshl_add_u64 v[10:11], v[10:11], 0, v[4:5]
	global_store_dwordx2 v[10:11], v[28:29], off
	s_nop 0
	v_mov_b32_e32 v14, v59
	v_mov_b32_e32 v16, v60
	v_mov_b32_e32 v18, v61
	v_mov_b32_e32 v20, v54
	v_mov_b32_e32 v22, v55
	v_mov_b32_e32 v24, v56
	v_mov_b32_e32 v28, 0
	v_mov_b32_e32 v29, 0
	v_mov_b32_e32 v26, v57
	v_add_u32_e32 v30, 0xa0, v2
	s_waitcnt vmcnt(7)
; __device__ __forceinline__ float sigm(float x) { return __builtin_amdgcn_rcpf(1.f + __builtin_amdgcn_exp2f(-1.4426950408889634f * x)); }
; __device__ __forceinline__ unsigned pk4_fp8(float a, float b, float c, float d) { int w = 0; w = __builtin_amdgcn_cvt_pk_fp8_f32(a, b, w, false); w = __builtin_amdgcn_cvt_pk_fp8_f32(c, d, w, true); return (unsigned)w; }
; __device__ __forceinline__ u32x4 pack8(f32x4 v0, f32x4 v1) { u32x4 w; w.x = cvt_pk_bf16(v0[0], v0[1]); w.y = cvt_pk_bf16(v0[2], v0[3]); w.z = cvt_pk_bf16(v1[0], v1[1]); w.w = cvt_pk_bf16(v1[2], v1[3]); return w; }
; template <class T> __device__ __forceinline__ void est(T* p, T v) { if constexpr (MK_EPI_NT != 0) __builtin_nontemporal_store(v, p); else *p = v; }
; __device__ __forceinline__ float ss_val(const ss_t* ss, int row) { return (float)ss[row] * (1.f / 16777216.f); }
;     ...
;         if constexpr (Epi::KEEP) keep = E(acc, cur, wr, wc, fr, fq); else E(acc, cur, wr, wc, fr, fq);
;         if (!has_next) break;
;     __device__ __forceinline__ void operator()(AccT acc, const Unit& u, int wr, int wc, int fr, int fq) const {
;         const int row0 = u.pm * 256 + wr * 64 + fr, col0 = u.pn * 128 + wc * 32 + 8 * fq;
; #pragma unroll
;         for (int ai = 0; ai < 2; ++ai)
; #pragma unroll
;             for (int m = 0; m < 4; ++m) { const int row = row0 + ai * 128 + m * 16; const float r = (is_rstd ? ((const float*)rs)[row] : rsqrtf(ss_val((const ss_t*)rs, row) * (1.0f / DM) + EPS)) * ascale;
;                 f32x4 o[2];
; #pragma unroll
;                 for (int bj = 0; bj < 2; ++bj) { const f32x4 a = acc[ai][bj][m][0] * r, b = acc[ai][bj][m][1] * r;
; #pragma unroll
;                     for (int j = 0; j < 4; ++j) o[bj][j] = a[j] * sigm(a[j]) * b[j]; }
;                 if constexpr (F8OUT) est((u32x2*)((unsigned char*)O + (size_t)row * ldo + col0), (u32x2)(u32x2){pk4_fp8(o[0][0], o[0][1], o[0][2], o[0][3]), pk4_fp8(o[1][0], o[1][1], o[1][2], o[1][3])});
;                 else est((u32x4*)((bf16_t*)O + (size_t)row * ldo + col0), (u32x4)pack8(o[0], o[1])); }
;     }
	v_mov_b32_e32 v3, v254
	v_mul_f32_e32 v10, 0x3d000000, v3
	v_mul_f32_e32 v11, v62, v10
	v_mul_f32_e32 v3, 0xbfb8aa3b, v11
	v_exp_f32_e32 v3, v3
	s_nop 0
	v_add_f32_e32 v3, 1.0, v3
	v_rcp_f32_e32 v13, v3
	s_nop 0
	v_pk_mul_f32 v[12:13], v[12:13], v[10:11]
	v_mul_f32_e32 v11, v63, v10
	v_mul_f32_e32 v3, 0xbfb8aa3b, v11
	v_exp_f32_e32 v3, v3
	v_mul_f32_e32 v12, v12, v13
	v_add_f32_e32 v3, 1.0, v3
	v_rcp_f32_e32 v15, v3
	s_nop 0
	v_pk_mul_f32 v[14:15], v[14:15], v[10:11]
	v_mul_f32_e32 v11, v64, v10
	v_mul_f32_e32 v3, 0xbfb8aa3b, v11
	v_exp_f32_e32 v3, v3
	s_nop 0
	v_add_f32_e32 v3, 1.0, v3
	v_rcp_f32_e32 v17, v3
	s_nop 0
	v_pk_mul_f32 v[16:17], v[16:17], v[10:11]
	v_mul_f32_e32 v11, v65, v10
	v_mul_f32_e32 v3, 0xbfb8aa3b, v11
	v_exp_f32_e32 v3, v3
	s_nop 0
	v_add_f32_e32 v3, 1.0, v3
	v_rcp_f32_e32 v19, v3
	s_nop 0
	v_pk_mul_f32 v[18:19], v[18:19], v[10:11]
	v_mul_f32_e32 v11, v50, v10
	v_mul_f32_e32 v3, 0xbfb8aa3b, v11
	v_exp_f32_e32 v3, v3
	s_nop 0
	v_add_f32_e32 v3, 1.0, v3
	v_rcp_f32_e32 v21, v3
	s_nop 0
	v_pk_mul_f32 v[20:21], v[20:21], v[10:11]
	v_mul_f32_e32 v11, v51, v10
	v_mul_f32_e32 v3, 0xbfb8aa3b, v11
	v_exp_f32_e32 v3, v3
	s_nop 0
	v_add_f32_e32 v3, 1.0, v3
	v_rcp_f32_e32 v23, v3
	s_nop 0
	v_pk_mul_f32 v[22:23], v[22:23], v[10:11]
	v_mul_f32_e32 v11, v52, v10
	v_mul_f32_e32 v3, 0xbfb8aa3b, v11
	v_exp_f32_e32 v3, v3
	s_nop 0
	v_add_f32_e32 v3, 1.0, v3
	v_rcp_f32_e32 v25, v3
	v_mul_f32_e32 v3, v14, v15
	v_cvt_pk_fp8_f32 v28, v12, v3
	v_mul_f32_e32 v3, v16, v17
	v_pk_mul_f32 v[12:13], v[24:25], v[10:11]
	v_mul_f32_e32 v11, v53, v10
	v_mul_f32_e32 v14, 0xbfb8aa3b, v11
	v_exp_f32_e32 v14, v14
	v_mul_f32_e32 v15, v18, v19
	v_cvt_pk_fp8_f32 v28, v3, v15 op_sel:[0,0,1]
	v_mul_f32_e32 v3, v20, v21
	v_add_f32_e32 v14, 1.0, v14
	v_rcp_f32_e32 v27, v14
	v_mul_f32_e32 v14, v22, v23
	v_cvt_pk_fp8_f32 v29, v3, v14
	v_mul_f32_e32 v3, v12, v13
	v_pk_mul_f32 v[10:11], v[26:27], v[10:11]
	v_mov_b32_e32 v12, v43
	v_mul_f32_e32 v10, v10, v11
	v_cvt_pk_fp8_f32 v29, v3, v10 op_sel:[0,0,1]
	v_mad_i64_i32 v[10:11], s[64:65], v30, s71, v[6:7]
	v_lshl_add_u64 v[10:11], v[10:11], 0, v[4:5]
	global_store_dwordx2 v[10:11], v[28:29], off
	s_nop 0
	v_mov_b32_e32 v10, v42
	v_mov_b32_e32 v14, v44
	v_mov_b32_e32 v16, v45
	v_mov_b32_e32 v18, v38
	v_mov_b32_e32 v20, v39
	v_mov_b32_e32 v22, v40
	v_mov_b32_e32 v26, 0
	v_add_u32_e32 v28, 0xb0, v2
	v_mov_b32_e32 v27, 0
	v_mov_b32_e32 v24, v41
	s_waitcnt vmcnt(7)
	v_mov_b32_e32 v3, v255
	v_mul_f32_e32 v8, 0x3d000000, v3
	v_mul_f32_e32 v9, v46, v8
	v_mul_f32_e32 v3, 0xbfb8aa3b, v9
	v_exp_f32_e32 v3, v3
	s_nop 0
	v_add_f32_e32 v3, 1.0, v3
	v_rcp_f32_e32 v11, v3
	s_nop 0
	v_pk_mul_f32 v[10:11], v[10:11], v[8:9]
	v_mul_f32_e32 v9, v47, v8
	v_mul_f32_e32 v3, 0xbfb8aa3b, v9
	v_exp_f32_e32 v3, v3
	v_mul_f32_e32 v2, v10, v11
	v_add_f32_e32 v3, 1.0, v3
	v_rcp_f32_e32 v13, v3
	s_nop 0
	v_pk_mul_f32 v[12:13], v[12:13], v[8:9]
	v_mul_f32_e32 v9, v48, v8
	v_mul_f32_e32 v3, 0xbfb8aa3b, v9
	v_exp_f32_e32 v3, v3
	s_nop 0
	v_add_f32_e32 v3, 1.0, v3
	v_rcp_f32_e32 v15, v3
	s_nop 0
	v_pk_mul_f32 v[14:15], v[14:15], v[8:9]
	v_mul_f32_e32 v9, v49, v8
	v_mul_f32_e32 v3, 0xbfb8aa3b, v9
	v_exp_f32_e32 v3, v3
	v_mul_f32_e32 v10, v14, v15
	v_add_f32_e32 v3, 1.0, v3
	v_rcp_f32_e32 v17, v3
	s_nop 0
	v_pk_mul_f32 v[16:17], v[16:17], v[8:9]
	v_mul_f32_e32 v9, v34, v8
	v_mul_f32_e32 v3, 0xbfb8aa3b, v9
	v_exp_f32_e32 v3, v3
	s_nop 0
	v_add_f32_e32 v3, 1.0, v3
	v_rcp_f32_e32 v19, v3
	s_nop 0
	v_pk_mul_f32 v[18:19], v[18:19], v[8:9]
	v_mul_f32_e32 v9, v35, v8
	v_mul_f32_e32 v3, 0xbfb8aa3b, v9
	v_exp_f32_e32 v3, v3
	s_nop 0
	v_add_f32_e32 v3, 1.0, v3
	v_rcp_f32_e32 v21, v3
	s_nop 0
	v_pk_mul_f32 v[20:21], v[20:21], v[8:9]
	v_mul_f32_e32 v9, v36, v8
	v_mul_f32_e32 v3, 0xbfb8aa3b, v9
	v_exp_f32_e32 v3, v3
	s_nop 0
	v_add_f32_e32 v3, 1.0, v3
	v_rcp_f32_e32 v23, v3
	v_mul_f32_e32 v3, v12, v13
	v_cvt_pk_fp8_f32 v26, v2, v3
	v_mul_f32_e32 v12, v16, v17
	v_pk_mul_f32 v[2:3], v[22:23], v[8:9]
	v_mul_f32_e32 v9, v37, v8
	v_mul_f32_e32 v11, 0xbfb8aa3b, v9
	v_exp_f32_e32 v11, v11
	v_cvt_pk_fp8_f32 v26, v10, v12 op_sel:[0,0,1]
	v_mul_f32_e32 v10, v18, v19
	v_add_f32_e32 v11, 1.0, v11
	v_rcp_f32_e32 v25, v11
	v_mul_f32_e32 v11, v20, v21
	v_cvt_pk_fp8_f32 v27, v10, v11
	v_mul_f32_e32 v10, v2, v3
	v_pk_mul_f32 v[2:3], v[24:25], v[8:9]
	s_nop 0
	v_mul_f32_e32 v2, v2, v3
	v_cvt_pk_fp8_f32 v27, v10, v2 op_sel:[0,0,1]
	v_mad_i64_i32 v[2:3], s[64:65], v28, s71, v[6:7]
	v_lshl_add_u64 v[2:3], v[2:3], 0, v[4:5]
	global_store_dwordx2 v[2:3], v[26:27], off
	s_cbranch_vccnz .LBB0_2254
	s_andn2_b64 vcc, exec, s[22:23]
	s_cbranch_vccnz .LBB0_2253
	s_barrier
	s_branch .LBB0_2253

; __device__ __forceinline__ u32x4 pack8(f32x4 v0, f32x4 v1) { u32x4 w; w.x = cvt_pk_bf16(v0[0], v0[1]); w.y = cvt_pk_bf16(v0[2], v0[3]); w.z = cvt_pk_bf16(v1[0], v1[1]); w.w = cvt_pk_bf16(v1[2], v1[3]); return w; }
; template <class T> __device__ __forceinline__ void est(T* p, T v) { if constexpr (MK_EPI_NT != 0) __builtin_nontemporal_store(v, p); else *p = v; }
;     __device__ __forceinline__ void operator()(AccT acc, const Unit& u, int wr, int wc, int fr, int fq) const {
;         const int row0 = u.pm * 256 + wr * 64 + fr, col0 = u.pn * 256 + wc * 32 + 8 * fq;
; #pragma unroll
;         for (int ai = 0; ai < 2; ++ai)
; #pragma unroll
;             for (int m = 0; m < 4; ++m) { const int row = row0 + ai * 128 + m * 16; const float g = row_gate[row] * ascale; bf16_t* rp = (u.z == 0 ? YB + (size_t)row * DM : YBX + ((size_t)(u.z - 1) * 2048 + (row - 16384)) * DM) + col0;
; #pragma unroll
;                 for (int bj = 0; bj < 2; ++bj) est((u32x4*)(rp + bj * 128), (u32x4)pack8(acc[ai][bj][m][0] * g, acc[ai][bj][m][1] * g)); }
;     }
.LBB0_2338:
	v_lshl_add_u32 v6, s66, 8, v163
	v_ashrrev_i32_e32 v7, 31, v6
	s_nop 15
	s_nop 15
	v_lshl_add_u64 v[2:3], v[6:7], 2, s[6:7]
	global_load_dword v248, v[2:3], off
	global_load_dword v249, v[2:3], off offset:64
	global_load_dword v250, v[2:3], off offset:128
	global_load_dword v251, v[2:3], off offset:192
	global_load_dword v252, v[2:3], off offset:512
	global_load_dword v253, v[2:3], off offset:576
	global_load_dword v254, v[2:3], off offset:640
	global_load_dword v255, v[2:3], off offset:704
	v_lshl_or_b32 v4, s79, 8, v202
	v_ashrrev_i32_e32 v5, 31, v4
	v_lshlrev_b64 v[8:9], 12, v[6:7]
	v_lshlrev_b64 v[14:15], 1, v[4:5]
	v_lshl_add_u64 v[4:5], s[14:15], 0, v[8:9]
	v_or_b32_e32 v12, 16, v6
	v_ashrrev_i32_e32 v13, 31, v12
	v_lshl_add_u64 v[4:5], v[4:5], 0, v[14:15]
	v_lshl_add_u64 v[16:17], v[12:13], 2, s[6:7]
	s_waitcnt vmcnt(7)
	v_mov_b32_e32 v10, v248
	v_mul_f32_e32 v8, 0x3c800000, v10
	v_pk_mul_f32 v[10:11], v[160:161], v[8:9] op_sel_hi:[1,0]
	v_pk_mul_f32 v[18:19], v[158:159], v[8:9] op_sel_hi:[1,0]
	v_pk_mul_f32 v[20:21], v[156:157], v[8:9] op_sel_hi:[1,0]
	v_pk_mul_f32 v[22:23], v[154:155], v[8:9] op_sel_hi:[1,0]
	v_pk_mul_f32 v[24:25], v[152:153], v[8:9] op_sel_hi:[1,0]
	v_pk_mul_f32 v[26:27], v[150:151], v[8:9] op_sel_hi:[1,0]
	v_pk_mul_f32 v[28:29], v[148:149], v[8:9] op_sel_hi:[1,0]
	v_pk_mul_f32 v[30:31], v[146:147], v[8:9] op_sel_hi:[1,0]
	v_cvt_pk_bf16_f32 v8, v18, v19
	v_cvt_pk_bf16_f32 v9, v10, v11
	v_cvt_pk_bf16_f32 v10, v22, v23
	v_cvt_pk_bf16_f32 v11, v20, v21
	global_store_dwordx4 v[4:5], v[8:11], off
	s_nop 1
	v_cvt_pk_bf16_f32 v8, v26, v27
	v_cvt_pk_bf16_f32 v9, v24, v25
	v_cvt_pk_bf16_f32 v10, v30, v31
	v_cvt_pk_bf16_f32 v11, v28, v29
	global_store_dwordx4 v[4:5], v[8:11], off offset:256
	s_nop 0
	v_or_b32_e32 v16, 32, v6
	v_lshlrev_b64 v[8:9], 12, v[12:13]
	v_lshl_add_u64 v[8:9], s[14:15], 0, v[8:9]
	v_lshl_add_u64 v[18:19], v[8:9], 0, v[14:15]
	v_ashrrev_i32_e32 v17, 31, v16
	v_lshl_add_u64 v[12:13], v[16:17], 2, s[6:7]
	s_waitcnt vmcnt(8)
	v_mov_b32_e32 v7, v249
	v_mul_f32_e32 v8, 0x3c800000, v7
	v_pk_mul_f32 v[10:11], v[144:145], v[8:9] op_sel_hi:[1,0]
	v_pk_mul_f32 v[20:21], v[142:143], v[8:9] op_sel_hi:[1,0]
	v_pk_mul_f32 v[22:23], v[140:141], v[8:9] op_sel_hi:[1,0]
	v_pk_mul_f32 v[24:25], v[138:139], v[8:9] op_sel_hi:[1,0]
	v_pk_mul_f32 v[26:27], v[136:137], v[8:9] op_sel_hi:[1,0]
	v_pk_mul_f32 v[28:29], v[134:135], v[8:9] op_sel_hi:[1,0]
	v_pk_mul_f32 v[30:31], v[132:133], v[8:9] op_sel_hi:[1,0]
	v_pk_mul_f32 v[32:33], v[130:131], v[8:9] op_sel_hi:[1,0]
	v_cvt_pk_bf16_f32 v8, v20, v21
	v_cvt_pk_bf16_f32 v9, v10, v11
	v_cvt_pk_bf16_f32 v10, v24, v25
	v_cvt_pk_bf16_f32 v11, v22, v23
	global_store_dwordx4 v[18:19], v[8:11], off
	s_nop 1
	v_cvt_pk_bf16_f32 v8, v28, v29
	v_cvt_pk_bf16_f32 v9, v26, v27
	v_cvt_pk_bf16_f32 v10, v32, v33
	v_cvt_pk_bf16_f32 v11, v30, v31
	global_store_dwordx4 v[18:19], v[8:11], off offset:256
	s_nop 0
	s_nop 0
	v_or_b32_e32 v10, 48, v6
	v_lshlrev_b64 v[6:7], 12, v[16:17]
	v_lshl_add_u64 v[6:7], s[14:15], 0, v[6:7]
	v_lshl_add_u64 v[16:17], v[6:7], 0, v[14:15]
	v_ashrrev_i32_e32 v11, 31, v10
	v_lshl_add_u64 v[12:13], v[10:11], 2, s[6:7]
	s_waitcnt vmcnt(9)
	v_mov_b32_e32 v8, v250
	v_mul_f32_e32 v6, 0x3c800000, v8
	v_pk_mul_f32 v[8:9], v[128:129], v[6:7] op_sel_hi:[1,0]
	v_pk_mul_f32 v[18:19], v[126:127], v[6:7] op_sel_hi:[1,0]
	v_pk_mul_f32 v[20:21], v[124:125], v[6:7] op_sel_hi:[1,0]
	v_pk_mul_f32 v[22:23], v[122:123], v[6:7] op_sel_hi:[1,0]
	v_pk_mul_f32 v[24:25], v[120:121], v[6:7] op_sel_hi:[1,0]
	v_pk_mul_f32 v[26:27], v[118:119], v[6:7] op_sel_hi:[1,0]
	v_pk_mul_f32 v[28:29], v[116:117], v[6:7] op_sel_hi:[1,0]
	v_pk_mul_f32 v[30:31], v[114:115], v[6:7] op_sel_hi:[1,0]
	v_cvt_pk_bf16_f32 v6, v18, v19
	v_cvt_pk_bf16_f32 v7, v8, v9
	v_cvt_pk_bf16_f32 v8, v22, v23
	v_cvt_pk_bf16_f32 v9, v20, v21
	global_store_dwordx4 v[16:17], v[6:9], off
	s_nop 1
	v_cvt_pk_bf16_f32 v6, v26, v27
	v_cvt_pk_bf16_f32 v7, v24, v25
	v_cvt_pk_bf16_f32 v8, v30, v31
	v_cvt_pk_bf16_f32 v9, v28, v29
	global_store_dwordx4 v[16:17], v[6:9], off offset:256
	s_nop 0
	s_nop 0
	v_lshlrev_b64 v[6:7], 12, v[10:11]
	v_lshl_add_u64 v[6:7], s[14:15], 0, v[6:7]
	v_lshl_add_u64 v[10:11], v[6:7], 0, v[14:15]
	s_waitcnt vmcnt(10)
; __device__ __forceinline__ u32x4 pack8(f32x4 v0, f32x4 v1) { u32x4 w; w.x = cvt_pk_bf16(v0[0], v0[1]); w.y = cvt_pk_bf16(v0[2], v0[3]); w.z = cvt_pk_bf16(v1[0], v1[1]); w.w = cvt_pk_bf16(v1[2], v1[3]); return w; }
; template <class T> __device__ __forceinline__ void est(T* p, T v) { if constexpr (MK_EPI_NT != 0) __builtin_nontemporal_store(v, p); else *p = v; }
;     ...
;         if constexpr (Epi::KEEP) keep = E(acc, cur, wr, wc, fr, fq); else E(acc, cur, wr, wc, fr, fq);
;         if (!has_next) break;
;     __device__ __forceinline__ void operator()(AccT acc, const Unit& u, int wr, int wc, int fr, int fq) const {
;         const int row0 = u.pm * 256 + wr * 64 + fr, col0 = u.pn * 256 + wc * 32 + 8 * fq;
; #pragma unroll
;         for (int ai = 0; ai < 2; ++ai)
; #pragma unroll
;             for (int m = 0; m < 4; ++m) { const int row = row0 + ai * 128 + m * 16; const float g = row_gate[row] * ascale; bf16_t* rp = (u.z == 0 ? YB + (size_t)row * DM : YBX + ((size_t)(u.z - 1) * 2048 + (row - 16384)) * DM) + col0;
; #pragma unroll
;                 for (int bj = 0; bj < 2; ++bj) est((u32x4*)(rp + bj * 128), (u32x4)pack8(acc[ai][bj][m][0] * g, acc[ai][bj][m][1] * g)); }
;     }
	v_mov_b32_e32 v8, v251
	v_mul_f32_e32 v6, 0x3c800000, v8
	v_pk_mul_f32 v[8:9], v[112:113], v[6:7] op_sel_hi:[1,0]
	v_pk_mul_f32 v[12:13], v[110:111], v[6:7] op_sel_hi:[1,0]
	v_pk_mul_f32 v[14:15], v[108:109], v[6:7] op_sel_hi:[1,0]
	v_pk_mul_f32 v[16:17], v[106:107], v[6:7] op_sel_hi:[1,0]
	v_pk_mul_f32 v[18:19], v[104:105], v[6:7] op_sel_hi:[1,0]
	v_pk_mul_f32 v[20:21], v[102:103], v[6:7] op_sel_hi:[1,0]
	v_pk_mul_f32 v[22:23], v[100:101], v[6:7] op_sel_hi:[1,0]
	v_pk_mul_f32 v[24:25], v[98:99], v[6:7] op_sel_hi:[1,0]
	v_cvt_pk_bf16_f32 v6, v12, v13
	v_cvt_pk_bf16_f32 v7, v8, v9
	v_cvt_pk_bf16_f32 v8, v16, v17
	v_cvt_pk_bf16_f32 v9, v14, v15
	global_store_dwordx4 v[10:11], v[6:9], off
	v_add_co_u32_e32 v12, vcc, s74, v4
	s_nop 0
	v_cvt_pk_bf16_f32 v6, v20, v21
	v_cvt_pk_bf16_f32 v7, v18, v19
	v_cvt_pk_bf16_f32 v8, v24, v25
	v_cvt_pk_bf16_f32 v9, v22, v23
	global_store_dwordx4 v[10:11], v[6:9], off offset:256
	s_nop 0
	v_lshl_add_u64 v[10:11], v[4:5], 0, s[38:39]
	v_addc_co_u32_e32 v13, vcc, 0, v5, vcc
	s_waitcnt vmcnt(11)
	v_mov_b32_e32 v6, v252
	v_mul_f32_e32 v6, 0x3c800000, v6
	v_pk_mul_f32 v[8:9], v[96:97], v[6:7] op_sel_hi:[1,0]
	v_pk_mul_f32 v[14:15], v[94:95], v[6:7] op_sel_hi:[1,0]
	v_pk_mul_f32 v[16:17], v[92:93], v[6:7] op_sel_hi:[1,0]
	v_pk_mul_f32 v[18:19], v[90:91], v[6:7] op_sel_hi:[1,0]
	v_pk_mul_f32 v[20:21], v[88:89], v[6:7] op_sel_hi:[1,0]
	v_pk_mul_f32 v[22:23], v[86:87], v[6:7] op_sel_hi:[1,0]
	v_pk_mul_f32 v[24:25], v[84:85], v[6:7] op_sel_hi:[1,0]
	v_pk_mul_f32 v[26:27], v[82:83], v[6:7] op_sel_hi:[1,0]
	v_cvt_pk_bf16_f32 v6, v14, v15
	v_cvt_pk_bf16_f32 v7, v8, v9
	v_cvt_pk_bf16_f32 v8, v18, v19
	v_cvt_pk_bf16_f32 v9, v16, v17
	global_store_dwordx4 v[12:13], v[6:9], off
	v_add_co_u32_e32 v12, vcc, s75, v4
	s_nop 0
	v_cvt_pk_bf16_f32 v6, v22, v23
	v_cvt_pk_bf16_f32 v7, v20, v21
	v_cvt_pk_bf16_f32 v8, v26, v27
	v_cvt_pk_bf16_f32 v9, v24, v25
	global_store_dwordx4 v[10:11], v[6:9], off offset:256
	s_nop 0
	v_lshl_add_u64 v[10:11], v[4:5], 0, s[40:41]
	v_addc_co_u32_e32 v13, vcc, 0, v5, vcc
	s_waitcnt vmcnt(12)
	v_mov_b32_e32 v6, v253
	v_mul_f32_e32 v6, 0x3c800000, v6
	v_pk_mul_f32 v[8:9], v[80:81], v[6:7] op_sel_hi:[1,0]
	v_pk_mul_f32 v[14:15], v[78:79], v[6:7] op_sel_hi:[1,0]
	v_pk_mul_f32 v[16:17], v[76:77], v[6:7] op_sel_hi:[1,0]
	v_pk_mul_f32 v[18:19], v[74:75], v[6:7] op_sel_hi:[1,0]
	v_pk_mul_f32 v[20:21], v[72:73], v[6:7] op_sel_hi:[1,0]
	v_pk_mul_f32 v[22:23], v[70:71], v[6:7] op_sel_hi:[1,0]
	v_pk_mul_f32 v[24:25], v[68:69], v[6:7] op_sel_hi:[1,0]
	v_pk_mul_f32 v[26:27], v[66:67], v[6:7] op_sel_hi:[1,0]
	v_cvt_pk_bf16_f32 v6, v14, v15
	v_cvt_pk_bf16_f32 v7, v8, v9
	v_cvt_pk_bf16_f32 v8, v18, v19
	v_cvt_pk_bf16_f32 v9, v16, v17
	global_store_dwordx4 v[12:13], v[6:9], off
	v_add_co_u32_e32 v12, vcc, s76, v4
	s_nop 0
	v_cvt_pk_bf16_f32 v6, v22, v23
	v_cvt_pk_bf16_f32 v7, v20, v21
	v_cvt_pk_bf16_f32 v8, v26, v27
	v_cvt_pk_bf16_f32 v9, v24, v25
	global_store_dwordx4 v[10:11], v[6:9], off offset:256
	s_nop 0
	v_lshl_add_u64 v[10:11], v[4:5], 0, s[46:47]
	v_addc_co_u32_e32 v13, vcc, 0, v5, vcc
	s_andn2_b64 vcc, exec, s[4:5]
	s_waitcnt vmcnt(13)
	v_mov_b32_e32 v6, v254
	v_mul_f32_e32 v6, 0x3c800000, v6
	v_pk_mul_f32 v[8:9], v[64:65], v[6:7] op_sel_hi:[1,0]
	v_pk_mul_f32 v[14:15], v[62:63], v[6:7] op_sel_hi:[1,0]
	v_pk_mul_f32 v[16:17], v[60:61], v[6:7] op_sel_hi:[1,0]
	v_pk_mul_f32 v[18:19], v[58:59], v[6:7] op_sel_hi:[1,0]
	v_pk_mul_f32 v[20:21], v[56:57], v[6:7] op_sel_hi:[1,0]
	v_pk_mul_f32 v[22:23], v[54:55], v[6:7] op_sel_hi:[1,0]
	v_pk_mul_f32 v[24:25], v[52:53], v[6:7] op_sel_hi:[1,0]
	v_pk_mul_f32 v[26:27], v[50:51], v[6:7] op_sel_hi:[1,0]
	v_cvt_pk_bf16_f32 v6, v14, v15
	v_cvt_pk_bf16_f32 v7, v8, v9
	v_cvt_pk_bf16_f32 v8, v18, v19
	v_cvt_pk_bf16_f32 v9, v16, v17
	global_store_dwordx4 v[12:13], v[6:9], off
	s_nop 1
	v_cvt_pk_bf16_f32 v6, v22, v23
	v_cvt_pk_bf16_f32 v7, v20, v21
	v_cvt_pk_bf16_f32 v8, v26, v27
	v_cvt_pk_bf16_f32 v9, v24, v25
	global_store_dwordx4 v[10:11], v[6:9], off offset:256
	s_nop 0
	s_waitcnt vmcnt(14)
	v_mov_b32_e32 v2, v255
	v_mul_f32_e32 v2, 0x3c800000, v2
	v_add_co_u32_e64 v8, s[4:5], s77, v4
	v_lshl_add_u64 v[6:7], v[4:5], 0, s[48:49]
	s_nop 0
	v_addc_co_u32_e64 v9, s[4:5], 0, v5, s[4:5]
	v_pk_mul_f32 v[4:5], v[48:49], v[2:3] op_sel_hi:[1,0]
	v_pk_mul_f32 v[10:11], v[46:47], v[2:3] op_sel_hi:[1,0]
	v_pk_mul_f32 v[12:13], v[44:45], v[2:3] op_sel_hi:[1,0]
	v_pk_mul_f32 v[14:15], v[42:43], v[2:3] op_sel_hi:[1,0]
	v_pk_mul_f32 v[16:17], v[40:41], v[2:3] op_sel_hi:[1,0]
	v_pk_mul_f32 v[18:19], v[38:39], v[2:3] op_sel_hi:[1,0]
	v_pk_mul_f32 v[20:21], v[36:37], v[2:3] op_sel_hi:[1,0]
	v_pk_mul_f32 v[22:23], v[34:35], v[2:3] op_sel_hi:[1,0]
	v_cvt_pk_bf16_f32 v2, v10, v11
	v_cvt_pk_bf16_f32 v3, v4, v5
	v_cvt_pk_bf16_f32 v4, v14, v15
	v_cvt_pk_bf16_f32 v5, v12, v13
	s_mov_b64 s[4:5], -1
	global_store_dwordx4 v[8:9], v[2:5], off
	s_nop 1
	v_cvt_pk_bf16_f32 v2, v18, v19
	v_cvt_pk_bf16_f32 v3, v16, v17
	v_cvt_pk_bf16_f32 v4, v22, v23
	v_cvt_pk_bf16_f32 v5, v20, v21
	global_store_dwordx4 v[6:7], v[2:5], off offset:256
	s_cbranch_vccnz .LBB0_2326
	s_andn2_b64 vcc, exec, s[24:25]
	s_cbranch_vccnz .LBB0_2325
	s_barrier
	s_branch .LBB0_2325

; __device__ __forceinline__ u32x4 pack8(f32x4 v0, f32x4 v1) { u32x4 w; w.x = cvt_pk_bf16(v0[0], v0[1]); w.y = cvt_pk_bf16(v0[2], v0[3]); w.z = cvt_pk_bf16(v1[0], v1[1]); w.w = cvt_pk_bf16(v1[2], v1[3]); return w; }
; template <class T> __device__ __forceinline__ void est(T* p, T v) { if constexpr (MK_EPI_NT != 0) __builtin_nontemporal_store(v, p); else *p = v; }
;     __device__ __forceinline__ void operator()(AccT acc, const Unit& u, int wr, int wc, int fr, int fq) const {
;         const int row0 = u.pm * 256 + wr * 64 + fr, col0 = u.pn * 256 + wc * 32 + 8 * fq;
; #pragma unroll
;         for (int ai = 0; ai < 2; ++ai)
; #pragma unroll
;             for (int m = 0; m < 4; ++m) { const int row = row0 + ai * 128 + m * 16; const float g = row_gate[row] * ascale; bf16_t* rp = (u.z == 0 ? YB + (size_t)row * DM : YBX + ((size_t)(u.z - 1) * 2048 + (row - 16384)) * DM) + col0;
; #pragma unroll
;                 for (int bj = 0; bj < 2; ++bj) est((u32x4*)(rp + bj * 128), (u32x4)pack8(acc[ai][bj][m][0] * g, acc[ai][bj][m][1] * g)); }
;     }
;     __device__ __forceinline__ bool next(int i, pg8::Unit& u) const {
;         const int ntl = tiles[0] - 64, q = i * G + c; if (q >= ntl * 32) return false;
;         int tt; pg8::tile_of(q >> 2, ntl, 8, tt, u.pn); u.pm = 64 + tt; u.z = q & 3; const int e = tiles[1 + u.pm];
;         u.A = A0 + (size_t)u.pm * tsA + (size_t)u.z * kqbytes; u.B = B0 + (size_t)e * estride + (size_t)u.pn * tsB + (size_t)u.z * kqbytes; return true;
;     }
.LBB0_2354:
	v_lshl_add_u32 v2, s68, 8, v198
	v_ashrrev_i32_e32 v3, 31, v2
	s_nop 15
	s_nop 15
	v_lshl_add_u64 v[4:5], v[2:3], 2, s[6:7]
	global_load_dword v248, v[4:5], off
	global_load_dword v249, v[4:5], off offset:64
	global_load_dword v250, v[4:5], off offset:128
	global_load_dword v251, v[4:5], off offset:192
	global_load_dword v252, v[4:5], off offset:512
	global_load_dword v253, v[4:5], off offset:576
	global_load_dword v254, v[4:5], off offset:640
	global_load_dword v255, v[4:5], off offset:704
	v_sub_co_u32_e64 v11, vcc, s66, 1
	s_nop 0
	v_readfirstlane_b32 s4, v11
	s_lshl_b64 s[40:41], s[4:5], 23
	v_add_u32_e32 v8, 0xffffc000, v2
	s_add_u32 s4, s51, s40
	v_ashrrev_i32_e32 v9, 31, v8
	s_addc_u32 s46, s56, s41
	v_lshl_or_b32 v6, s67, 8, v199
	v_cndmask_b32_e32 v9, v9, v3, vcc
	v_cndmask_b32_e32 v8, v8, v2, vcc
	s_and_b64 s[40:41], vcc, exec
	v_ashrrev_i32_e32 v7, 31, v6
	v_lshlrev_b64 v[8:9], 12, v[8:9]
	s_cselect_b32 s41, s15, s46
	s_cselect_b32 s40, s14, s4
	v_lshlrev_b64 v[6:7], 1, v[6:7]
	v_lshl_add_u64 v[8:9], s[40:41], 0, v[8:9]
	v_lshl_add_u64 v[16:17], v[8:9], 0, v[6:7]
	v_or_b32_e32 v12, 16, v2
	v_ashrrev_i32_e32 v13, 31, v12
	v_lshl_add_u64 v[14:15], v[12:13], 2, s[6:7]
	s_waitcnt vmcnt(7)
	v_mov_b32_e32 v10, v248
	v_mul_f32_e32 v8, 0x3c800000, v10
	v_pk_mul_f32 v[10:11], v[160:161], v[8:9] op_sel_hi:[1,0]
	v_pk_mul_f32 v[18:19], v[158:159], v[8:9] op_sel_hi:[1,0]
	v_pk_mul_f32 v[20:21], v[156:157], v[8:9] op_sel_hi:[1,0]
	v_pk_mul_f32 v[22:23], v[154:155], v[8:9] op_sel_hi:[1,0]
	v_pk_mul_f32 v[24:25], v[152:153], v[8:9] op_sel_hi:[1,0]
	v_pk_mul_f32 v[26:27], v[150:151], v[8:9] op_sel_hi:[1,0]
	v_pk_mul_f32 v[28:29], v[148:149], v[8:9] op_sel_hi:[1,0]
	v_pk_mul_f32 v[30:31], v[146:147], v[8:9] op_sel_hi:[1,0]
	v_cvt_pk_bf16_f32 v8, v18, v19
	v_cvt_pk_bf16_f32 v9, v10, v11
	v_cvt_pk_bf16_f32 v10, v22, v23
	v_cvt_pk_bf16_f32 v11, v20, v21
	global_store_dwordx4 v[16:17], v[8:11], off
	s_nop 1
	v_cvt_pk_bf16_f32 v8, v26, v27
	v_cvt_pk_bf16_f32 v9, v24, v25
	v_cvt_pk_bf16_f32 v10, v30, v31
	v_cvt_pk_bf16_f32 v11, v28, v29
	global_store_dwordx4 v[16:17], v[8:11], off offset:256
	s_nop 0
	v_or_b32_e32 v14, 32, v2
	v_add_u32_e32 v8, 0xffffc010, v2
	v_ashrrev_i32_e32 v9, 31, v8
	v_cndmask_b32_e32 v9, v9, v13, vcc
	v_cndmask_b32_e32 v8, v8, v12, vcc
	v_lshlrev_b64 v[8:9], 12, v[8:9]
	v_lshl_add_u64 v[8:9], s[40:41], 0, v[8:9]
	v_lshl_add_u64 v[16:17], v[8:9], 0, v[6:7]
	v_ashrrev_i32_e32 v15, 31, v14
	v_lshl_add_u64 v[12:13], v[14:15], 2, s[6:7]
	s_waitcnt vmcnt(8)
	v_mov_b32_e32 v3, v249
	v_mul_f32_e32 v8, 0x3c800000, v3
	v_pk_mul_f32 v[10:11], v[144:145], v[8:9] op_sel_hi:[1,0]
	v_pk_mul_f32 v[18:19], v[142:143], v[8:9] op_sel_hi:[1,0]
	v_pk_mul_f32 v[20:21], v[140:141], v[8:9] op_sel_hi:[1,0]
	v_pk_mul_f32 v[22:23], v[138:139], v[8:9] op_sel_hi:[1,0]
	v_pk_mul_f32 v[24:25], v[136:137], v[8:9] op_sel_hi:[1,0]
	v_pk_mul_f32 v[26:27], v[134:135], v[8:9] op_sel_hi:[1,0]
	v_pk_mul_f32 v[28:29], v[132:133], v[8:9] op_sel_hi:[1,0]
	v_pk_mul_f32 v[30:31], v[130:131], v[8:9] op_sel_hi:[1,0]
	v_cvt_pk_bf16_f32 v8, v18, v19
	v_cvt_pk_bf16_f32 v9, v10, v11
	v_cvt_pk_bf16_f32 v10, v22, v23
	v_cvt_pk_bf16_f32 v11, v20, v21
	global_store_dwordx4 v[16:17], v[8:11], off
	s_nop 1
	v_cvt_pk_bf16_f32 v8, v26, v27
	v_cvt_pk_bf16_f32 v9, v24, v25
	v_cvt_pk_bf16_f32 v10, v30, v31
	v_cvt_pk_bf16_f32 v11, v28, v29
	global_store_dwordx4 v[16:17], v[8:11], off offset:256
	s_nop 0
	v_or_b32_e32 v12, 48, v2
	v_add_u32_e32 v8, 0xffffc020, v2
	v_ashrrev_i32_e32 v9, 31, v8
	v_cndmask_b32_e32 v9, v9, v15, vcc
	v_cndmask_b32_e32 v8, v8, v14, vcc
	v_lshlrev_b64 v[8:9], 12, v[8:9]
	v_lshl_add_u64 v[8:9], s[40:41], 0, v[8:9]
	v_lshl_add_u64 v[16:17], v[8:9], 0, v[6:7]
	v_ashrrev_i32_e32 v13, 31, v12
	v_lshl_add_u64 v[14:15], v[12:13], 2, s[6:7]
	s_waitcnt vmcnt(9)
	v_mov_b32_e32 v3, v250
	v_mul_f32_e32 v8, 0x3c800000, v3
	v_pk_mul_f32 v[10:11], v[128:129], v[8:9] op_sel_hi:[1,0]
	v_pk_mul_f32 v[18:19], v[126:127], v[8:9] op_sel_hi:[1,0]
	v_pk_mul_f32 v[20:21], v[124:125], v[8:9] op_sel_hi:[1,0]
	v_pk_mul_f32 v[22:23], v[122:123], v[8:9] op_sel_hi:[1,0]
	v_pk_mul_f32 v[24:25], v[120:121], v[8:9] op_sel_hi:[1,0]
	v_pk_mul_f32 v[26:27], v[118:119], v[8:9] op_sel_hi:[1,0]
	v_pk_mul_f32 v[28:29], v[112:113], v[8:9] op_sel_hi:[1,0]
	v_pk_mul_f32 v[30:31], v[110:111], v[8:9] op_sel_hi:[1,0]
	v_cvt_pk_bf16_f32 v8, v18, v19
	v_cvt_pk_bf16_f32 v9, v10, v11
	v_cvt_pk_bf16_f32 v10, v22, v23
	v_cvt_pk_bf16_f32 v11, v20, v21
	global_store_dwordx4 v[16:17], v[8:11], off
	s_nop 1
	v_cvt_pk_bf16_f32 v8, v26, v27
	v_cvt_pk_bf16_f32 v9, v24, v25
	v_cvt_pk_bf16_f32 v10, v30, v31
	v_cvt_pk_bf16_f32 v11, v28, v29
	global_store_dwordx4 v[16:17], v[8:11], off offset:256
	s_nop 0
	s_nop 0
	v_add_u32_e32 v8, 0xffffc030, v2
	v_ashrrev_i32_e32 v9, 31, v8
	v_cndmask_b32_e32 v9, v9, v13, vcc
	v_cndmask_b32_e32 v8, v8, v12, vcc
	v_lshlrev_b64 v[8:9], 12, v[8:9]
	v_lshl_add_u64 v[8:9], s[40:41], 0, v[8:9]
	v_lshl_add_u64 v[12:13], v[8:9], 0, v[6:7]
	s_waitcnt vmcnt(10)
; __device__ __forceinline__ u32x4 pack8(f32x4 v0, f32x4 v1) { u32x4 w; w.x = cvt_pk_bf16(v0[0], v0[1]); w.y = cvt_pk_bf16(v0[2], v0[3]); w.z = cvt_pk_bf16(v1[0], v1[1]); w.w = cvt_pk_bf16(v1[2], v1[3]); return w; }
; template <class T> __device__ __forceinline__ void est(T* p, T v) { if constexpr (MK_EPI_NT != 0) __builtin_nontemporal_store(v, p); else *p = v; }
;     ...
;         if constexpr (Epi::KEEP) keep = E(acc, cur, wr, wc, fr, fq); else E(acc, cur, wr, wc, fr, fq);
;         if (!has_next) break;
;     __device__ __forceinline__ void operator()(AccT acc, const Unit& u, int wr, int wc, int fr, int fq) const {
;         const int row0 = u.pm * 256 + wr * 64 + fr, col0 = u.pn * 256 + wc * 32 + 8 * fq;
; #pragma unroll
;         for (int ai = 0; ai < 2; ++ai)
; #pragma unroll
;             for (int m = 0; m < 4; ++m) { const int row = row0 + ai * 128 + m * 16; const float g = row_gate[row] * ascale; bf16_t* rp = (u.z == 0 ? YB + (size_t)row * DM : YBX + ((size_t)(u.z - 1) * 2048 + (row - 16384)) * DM) + col0;
; #pragma unroll
;                 for (int bj = 0; bj < 2; ++bj) est((u32x4*)(rp + bj * 128), (u32x4)pack8(acc[ai][bj][m][0] * g, acc[ai][bj][m][1] * g)); }
;     }
	v_mov_b32_e32 v3, v251
	v_mul_f32_e32 v8, 0x3c800000, v3
	v_pk_mul_f32 v[10:11], v[116:117], v[8:9] op_sel_hi:[1,0]
	v_pk_mul_f32 v[14:15], v[114:115], v[8:9] op_sel_hi:[1,0]
	v_pk_mul_f32 v[16:17], v[108:109], v[8:9] op_sel_hi:[1,0]
	v_pk_mul_f32 v[18:19], v[106:107], v[8:9] op_sel_hi:[1,0]
	v_pk_mul_f32 v[20:21], v[104:105], v[8:9] op_sel_hi:[1,0]
	v_pk_mul_f32 v[22:23], v[102:103], v[8:9] op_sel_hi:[1,0]
	v_pk_mul_f32 v[24:25], v[100:101], v[8:9] op_sel_hi:[1,0]
	v_pk_mul_f32 v[26:27], v[98:99], v[8:9] op_sel_hi:[1,0]
	v_cvt_pk_bf16_f32 v8, v14, v15
	v_cvt_pk_bf16_f32 v9, v10, v11
	v_cvt_pk_bf16_f32 v10, v18, v19
	v_cvt_pk_bf16_f32 v11, v16, v17
	global_store_dwordx4 v[12:13], v[8:11], off
	s_nop 1
	v_cvt_pk_bf16_f32 v8, v22, v23
	v_cvt_pk_bf16_f32 v9, v20, v21
	v_cvt_pk_bf16_f32 v10, v26, v27
	v_cvt_pk_bf16_f32 v11, v24, v25
	global_store_dwordx4 v[12:13], v[8:11], off offset:256
	s_nop 0
	s_nop 0
	v_add_u32_e32 v8, 0x80, v2
	v_add_u32_e32 v10, 0xffffc080, v2
	v_ashrrev_i32_e32 v9, 31, v8
	v_ashrrev_i32_e32 v11, 31, v10
	v_cndmask_b32_e32 v9, v11, v9, vcc
	v_cndmask_b32_e32 v8, v10, v8, vcc
	v_lshlrev_b64 v[8:9], 12, v[8:9]
	v_lshl_add_u64 v[8:9], s[40:41], 0, v[8:9]
	v_lshl_add_u64 v[12:13], v[8:9], 0, v[6:7]
	s_waitcnt vmcnt(11)
	v_mov_b32_e32 v3, v252
	v_mul_f32_e32 v8, 0x3c800000, v3
	v_pk_mul_f32 v[10:11], v[96:97], v[8:9] op_sel_hi:[1,0]
	v_pk_mul_f32 v[14:15], v[94:95], v[8:9] op_sel_hi:[1,0]
	v_pk_mul_f32 v[16:17], v[92:93], v[8:9] op_sel_hi:[1,0]
	v_pk_mul_f32 v[18:19], v[90:91], v[8:9] op_sel_hi:[1,0]
	v_pk_mul_f32 v[20:21], v[88:89], v[8:9] op_sel_hi:[1,0]
	v_pk_mul_f32 v[22:23], v[86:87], v[8:9] op_sel_hi:[1,0]
	v_pk_mul_f32 v[24:25], v[84:85], v[8:9] op_sel_hi:[1,0]
	v_pk_mul_f32 v[26:27], v[82:83], v[8:9] op_sel_hi:[1,0]
	v_cvt_pk_bf16_f32 v8, v14, v15
	v_cvt_pk_bf16_f32 v9, v10, v11
	v_cvt_pk_bf16_f32 v10, v18, v19
	v_cvt_pk_bf16_f32 v11, v16, v17
	global_store_dwordx4 v[12:13], v[8:11], off
	s_nop 1
	v_cvt_pk_bf16_f32 v8, v22, v23
	v_cvt_pk_bf16_f32 v9, v20, v21
	v_cvt_pk_bf16_f32 v10, v26, v27
	v_cvt_pk_bf16_f32 v11, v24, v25
	global_store_dwordx4 v[12:13], v[8:11], off offset:256
	s_nop 0
	s_nop 0
	v_add_u32_e32 v8, 0x90, v2
	v_add_u32_e32 v10, 0xffffc090, v2
	v_ashrrev_i32_e32 v9, 31, v8
	v_ashrrev_i32_e32 v11, 31, v10
	v_cndmask_b32_e32 v9, v11, v9, vcc
	v_cndmask_b32_e32 v8, v10, v8, vcc
	v_lshlrev_b64 v[8:9], 12, v[8:9]
	v_lshl_add_u64 v[8:9], s[40:41], 0, v[8:9]
	v_lshl_add_u64 v[12:13], v[8:9], 0, v[6:7]
	s_waitcnt vmcnt(12)
	v_mov_b32_e32 v3, v253
	v_mul_f32_e32 v8, 0x3c800000, v3
	v_pk_mul_f32 v[10:11], v[80:81], v[8:9] op_sel_hi:[1,0]
	v_pk_mul_f32 v[14:15], v[78:79], v[8:9] op_sel_hi:[1,0]
	v_pk_mul_f32 v[16:17], v[76:77], v[8:9] op_sel_hi:[1,0]
	v_pk_mul_f32 v[18:19], v[74:75], v[8:9] op_sel_hi:[1,0]
	v_pk_mul_f32 v[20:21], v[72:73], v[8:9] op_sel_hi:[1,0]
	v_pk_mul_f32 v[22:23], v[70:71], v[8:9] op_sel_hi:[1,0]
	v_pk_mul_f32 v[24:25], v[68:69], v[8:9] op_sel_hi:[1,0]
	v_pk_mul_f32 v[26:27], v[66:67], v[8:9] op_sel_hi:[1,0]
	v_cvt_pk_bf16_f32 v8, v14, v15
	v_cvt_pk_bf16_f32 v9, v10, v11
	v_cvt_pk_bf16_f32 v10, v18, v19
	v_cvt_pk_bf16_f32 v11, v16, v17
	global_store_dwordx4 v[12:13], v[8:11], off
	s_nop 1
	v_cvt_pk_bf16_f32 v8, v22, v23
	v_cvt_pk_bf16_f32 v9, v20, v21
	v_cvt_pk_bf16_f32 v10, v26, v27
	v_cvt_pk_bf16_f32 v11, v24, v25
	global_store_dwordx4 v[12:13], v[8:11], off offset:256
	s_nop 0
	s_nop 0
	v_add_u32_e32 v8, 0xa0, v2
	v_add_u32_e32 v10, 0xffffc0a0, v2
	v_ashrrev_i32_e32 v9, 31, v8
	v_ashrrev_i32_e32 v11, 31, v10
	v_cndmask_b32_e32 v9, v11, v9, vcc
	v_cndmask_b32_e32 v8, v10, v8, vcc
	v_lshlrev_b64 v[8:9], 12, v[8:9]
	v_lshl_add_u64 v[8:9], s[40:41], 0, v[8:9]
	v_lshl_add_u64 v[12:13], v[8:9], 0, v[6:7]
	s_waitcnt vmcnt(13)
	v_mov_b32_e32 v3, v254
	v_mul_f32_e32 v8, 0x3c800000, v3
	v_pk_mul_f32 v[10:11], v[64:65], v[8:9] op_sel_hi:[1,0]
	v_pk_mul_f32 v[14:15], v[62:63], v[8:9] op_sel_hi:[1,0]
	v_pk_mul_f32 v[16:17], v[60:61], v[8:9] op_sel_hi:[1,0]
	v_pk_mul_f32 v[18:19], v[58:59], v[8:9] op_sel_hi:[1,0]
	v_pk_mul_f32 v[20:21], v[56:57], v[8:9] op_sel_hi:[1,0]
	v_pk_mul_f32 v[22:23], v[54:55], v[8:9] op_sel_hi:[1,0]
	v_pk_mul_f32 v[24:25], v[52:53], v[8:9] op_sel_hi:[1,0]
	v_pk_mul_f32 v[26:27], v[50:51], v[8:9] op_sel_hi:[1,0]
	v_cvt_pk_bf16_f32 v8, v14, v15
	v_cvt_pk_bf16_f32 v9, v10, v11
	v_cvt_pk_bf16_f32 v10, v18, v19
	v_cvt_pk_bf16_f32 v11, v16, v17
	global_store_dwordx4 v[12:13], v[8:11], off
	s_nop 1
	v_cvt_pk_bf16_f32 v8, v22, v23
	v_cvt_pk_bf16_f32 v9, v20, v21
	v_cvt_pk_bf16_f32 v10, v26, v27
	v_cvt_pk_bf16_f32 v11, v24, v25
	global_store_dwordx4 v[12:13], v[8:11], off offset:256
	s_nop 0
	v_add_u32_e32 v5, 0xb0, v2
	v_add_u32_e32 v2, 0xffffc0b0, v2
	v_ashrrev_i32_e32 v3, 31, v5
	v_ashrrev_i32_e32 v8, 31, v2
	v_cndmask_b32_e32 v3, v8, v3, vcc
	v_cndmask_b32_e32 v2, v2, v5, vcc
	v_lshlrev_b64 v[2:3], 12, v[2:3]
	v_lshl_add_u64 v[2:3], s[40:41], 0, v[2:3]
	v_lshl_add_u64 v[6:7], v[2:3], 0, v[6:7]
	s_andn2_b64 vcc, exec, s[36:37]
	s_mov_b64 s[36:37], -1
	s_waitcnt vmcnt(14)
	v_mov_b32_e32 v4, v255
	v_mul_f32_e32 v2, 0x3c800000, v4
	v_pk_mul_f32 v[4:5], v[48:49], v[2:3] op_sel_hi:[1,0]
	v_pk_mul_f32 v[8:9], v[46:47], v[2:3] op_sel_hi:[1,0]
	v_pk_mul_f32 v[10:11], v[44:45], v[2:3] op_sel_hi:[1,0]
	v_pk_mul_f32 v[12:13], v[42:43], v[2:3] op_sel_hi:[1,0]
	v_pk_mul_f32 v[14:15], v[40:41], v[2:3] op_sel_hi:[1,0]
	v_pk_mul_f32 v[16:17], v[38:39], v[2:3] op_sel_hi:[1,0]
	v_pk_mul_f32 v[18:19], v[36:37], v[2:3] op_sel_hi:[1,0]
	v_pk_mul_f32 v[20:21], v[34:35], v[2:3] op_sel_hi:[1,0]
	v_cvt_pk_bf16_f32 v2, v8, v9
	v_cvt_pk_bf16_f32 v3, v4, v5
	v_cvt_pk_bf16_f32 v4, v12, v13
	v_cvt_pk_bf16_f32 v5, v10, v11
	global_store_dwordx4 v[6:7], v[2:5], off
	s_nop 1
	v_cvt_pk_bf16_f32 v2, v16, v17
	v_cvt_pk_bf16_f32 v3, v14, v15
	v_cvt_pk_bf16_f32 v4, v20, v21
	v_cvt_pk_bf16_f32 v5, v18, v19
	global_store_dwordx4 v[6:7], v[2:5], off offset:256
	s_cbranch_vccnz .LBB0_2347
	s_andn2_b64 vcc, exec, s[22:23]
	s_cbranch_vccnz .LBB0_2346
	s_barrier
	s_branch .LBB0_2346
